# speedup vs baseline: 1.0594x; 1.0065x over previous
.Lil_1:
	s_andn2_b64 vcc, exec, s[10:11]
	s_waitcnt lgkmcnt(0)
	v_mfma_f32_16x16x32_f16 v[34:37], v[38:41], v[46:49], v[106:109]
	s_add_i32 m0, s79, 0x1d800
	v_mfma_f32_16x16x32_f16 v[102:105], v[42:45], v[46:49], v[102:105]
	global_load_lds_dwordx4 v252, s[86:87]
	v_mfma_f32_16x16x32_f16 v[98:101], v[38:41], v[50:53], v[98:101]
	s_add_i32 m0, s79, 0x1f800
	v_mfma_f32_16x16x32_f16 v[94:97], v[42:45], v[50:53], v[94:97]
	global_load_lds_dwordx4 v253, s[86:87]
	ds_read_b128 v[46:49], v205 offset:12288
	ds_read_b128 v[50:53], v205 offset:14336
	v_mfma_f32_16x16x32_f16 v[2:5], v[38:41], v[6:9], v[138:141]
	s_add_i32 m0, s79, 0x21800
	v_mfma_f32_16x16x32_f16 v[6:9], v[42:45], v[6:9], v[134:137]
	global_load_lds_dwordx4 v254, s[86:87]
	v_mfma_f32_16x16x32_f16 v[10:13], v[38:41], v[14:17], v[130:133]
	s_add_i32 m0, s79, 0x23800
	v_mfma_f32_16x16x32_f16 v[14:17], v[42:45], v[14:17], v[126:129]
	global_load_lds_dwordx4 v255, s[86:87]
	ds_read_b128 v[248:251], v205 offset:16384
	v_mfma_f32_16x16x32_f16 v[18:21], v[38:41], v[22:25], v[122:125]
	s_add_i32 m0, s79, 0x19000
	v_mfma_f32_16x16x32_f16 v[22:25], v[42:45], v[22:25], v[118:121]
	global_load_lds_dwordx4 v224, s[88:89]
	v_mfma_f32_16x16x32_f16 v[26:29], v[38:41], v[30:33], v[114:117]
	s_add_i32 m0, s79, 0x1b000
	v_mfma_f32_16x16x32_f16 v[30:33], v[42:45], v[30:33], v[110:113]
	global_load_lds_dwordx4 v226, s[88:89]
	s_waitcnt lgkmcnt(1)
	v_mfma_f32_16x16x32_f16 v[90:93], v[38:41], v[46:49], v[90:93]
	v_mfma_f32_16x16x32_f16 v[86:89], v[42:45], v[46:49], v[86:89]
	v_cndmask_b32_e64 v46, 0, 1, s[10:11]
	v_cmp_ne_u32_e64 s[0:1], 1, v46
	v_mfma_f32_16x16x32_f16 v[106:109], v[38:41], v[50:53], v[142:145]
	v_mfma_f32_16x16x32_f16 v[82:85], v[42:45], v[50:53], v[82:85]
	s_cbranch_vccnz .LBB2_81
	s_branch .Lnine_1
.LBB2_79:
	s_andn2_b64 vcc, exec, s[10:11]
	s_waitcnt lgkmcnt(0)
	v_mfma_f32_16x16x32_f16 v[34:37], v[38:41], v[46:49], v[106:109]
	v_mfma_f32_16x16x32_f16 v[102:105], v[42:45], v[46:49], v[102:105]
	v_mfma_f32_16x16x32_f16 v[98:101], v[38:41], v[50:53], v[98:101]
	v_mfma_f32_16x16x32_f16 v[94:97], v[42:45], v[50:53], v[94:97]
	ds_read_b128 v[46:49], v205 offset:12288
	ds_read_b128 v[50:53], v205 offset:14336
	v_mfma_f32_16x16x32_f16 v[2:5], v[38:41], v[6:9], v[138:141]
	v_mfma_f32_16x16x32_f16 v[6:9], v[42:45], v[6:9], v[134:137]
	v_mfma_f32_16x16x32_f16 v[10:13], v[38:41], v[14:17], v[130:133]
	v_mfma_f32_16x16x32_f16 v[14:17], v[42:45], v[14:17], v[126:129]
	ds_read_b128 v[248:251], v205 offset:16384
	v_mfma_f32_16x16x32_f16 v[18:21], v[38:41], v[22:25], v[122:125]
	v_mfma_f32_16x16x32_f16 v[22:25], v[42:45], v[22:25], v[118:121]
	v_mfma_f32_16x16x32_f16 v[26:29], v[38:41], v[30:33], v[114:117]
	v_mfma_f32_16x16x32_f16 v[30:33], v[42:45], v[30:33], v[110:113]
	s_waitcnt lgkmcnt(1)
	v_mfma_f32_16x16x32_f16 v[90:93], v[38:41], v[46:49], v[90:93]
	v_mfma_f32_16x16x32_f16 v[86:89], v[42:45], v[46:49], v[86:89]
	v_cndmask_b32_e64 v46, 0, 1, s[10:11]
	v_cmp_ne_u32_e64 s[0:1], 1, v46
	v_mfma_f32_16x16x32_f16 v[106:109], v[38:41], v[50:53], v[142:145]
	v_mfma_f32_16x16x32_f16 v[82:85], v[42:45], v[50:53], v[82:85]
	s_cbranch_vccnz .LBB2_81
.Lnine_1:
	s_waitcnt lgkmcnt(0)
	v_mfma_f32_16x16x32_f16 v[70:73], v[38:41], v[248:251], v[70:73]
	v_mfma_f32_16x16x32_f16 v[78:81], v[42:45], v[248:251], v[78:81]
.LBB2_81:
	s_waitcnt lgkmcnt(0)
	ds_read_b128 v[110:113], v203 offset:18432
	ds_read_b128 v[114:117], v203 offset:20480
	ds_read_b128 v[38:41], v207
	ds_read_b128 v[42:45], v207 offset:2048
	ds_read_b128 v[232:235], v207 offset:4096
	ds_read_b128 v[236:239], v207 offset:6144
	ds_read_b128 v[240:243], v207 offset:8192
	ds_read_b128 v[244:247], v207 offset:10240
	s_and_b64 vcc, exec, s[0:1]
	s_waitcnt lgkmcnt(5)
	v_mfma_f32_16x16x32_f16 v[74:77], v[110:113], v[38:41], v[2:5]
	v_mfma_f32_16x16x32_f16 v[66:69], v[114:117], v[38:41], v[6:9]
	s_waitcnt lgkmcnt(4)
	v_mfma_f32_16x16x32_f16 v[62:65], v[110:113], v[42:45], v[10:13]
	v_mfma_f32_16x16x32_f16 v[58:61], v[114:117], v[42:45], v[14:17]
	s_waitcnt lgkmcnt(3)
	v_mfma_f32_16x16x32_f16 v[54:57], v[110:113], v[232:235], v[18:21]
	v_mfma_f32_16x16x32_f16 v[50:53], v[114:117], v[232:235], v[22:25]
	ds_read_b128 v[232:235], v207 offset:12288
	s_waitcnt lgkmcnt(3)
	v_mfma_f32_16x16x32_f16 v[46:49], v[110:113], v[236:239], v[26:29]
	v_mfma_f32_16x16x32_f16 v[42:45], v[114:117], v[236:239], v[30:33]
	ds_read_b128 v[236:239], v207 offset:14336
	s_waitcnt lgkmcnt(3)
	ds_read_b128 v[248:251], v207 offset:16384
	v_mfma_f32_16x16x32_f16 v[38:41], v[110:113], v[240:243], v[34:37]
	v_mfma_f32_16x16x32_f16 v[34:37], v[114:117], v[240:243], v[102:105]
	s_waitcnt lgkmcnt(3)
	v_mfma_f32_16x16x32_f16 v[30:33], v[110:113], v[244:247], v[98:101]
	v_mfma_f32_16x16x32_f16 v[26:29], v[114:117], v[244:247], v[94:97]
	s_waitcnt lgkmcnt(2)
	v_mfma_f32_16x16x32_f16 v[22:25], v[110:113], v[232:235], v[90:93]
	v_mfma_f32_16x16x32_f16 v[18:21], v[114:117], v[232:235], v[86:89]
	s_waitcnt lgkmcnt(1)
	v_mfma_f32_16x16x32_f16 v[14:17], v[110:113], v[236:239], v[106:109]
	v_mfma_f32_16x16x32_f16 v[10:13], v[114:117], v[236:239], v[82:85]
	s_cbranch_vccnz .LBB2_83
	s_waitcnt lgkmcnt(0)
	v_mfma_f32_16x16x32_f16 v[6:9], v[110:113], v[248:251], v[70:73]
	v_mfma_f32_16x16x32_f16 v[2:5], v[114:117], v[248:251], v[78:81]
	s_andn2_b64 vcc, exec, s[30:31]
	s_mov_b64 s[30:31], -1
	s_cbranch_vccnz .LBB2_67
	s_branch .LBB2_84

.Lil_2:
	s_and_b64 vcc, exec, s[0:1]
	s_waitcnt lgkmcnt(2)
	v_mfma_f32_16x16x32_f16 v[82:85], v[146:149], v[70:73], v[74:77]
	s_add_i32 m0, s79, 0x4800
	v_mfma_f32_16x16x32_f16 v[86:89], v[150:153], v[70:73], v[66:69]
	global_load_lds_dwordx4 v252, s[86:87]
	v_mfma_f32_16x16x32_f16 v[90:93], v[146:149], v[78:81], v[62:65]
	s_add_i32 m0, s79, 0x6800
	v_mfma_f32_16x16x32_f16 v[94:97], v[150:153], v[78:81], v[58:61]
	global_load_lds_dwordx4 v253, s[86:87]
	ds_read_b128 v[240:243], v205 offset:59392
	ds_read_b128 v[244:247], v205 offset:61440
	s_waitcnt lgkmcnt(2)
	v_mfma_f32_16x16x32_f16 v[98:101], v[146:149], v[232:235], v[54:57]
	s_add_i32 m0, s79, 0x8800
	v_mfma_f32_16x16x32_f16 v[102:105], v[150:153], v[232:235], v[50:53]
	global_load_lds_dwordx4 v254, s[86:87]
	v_mfma_f32_16x16x32_f16 v[106:109], v[146:149], v[236:239], v[46:49]
	s_add_i32 m0, s79, 0xa800
	v_mfma_f32_16x16x32_f16 v[110:113], v[150:153], v[236:239], v[42:45]
	global_load_lds_dwordx4 v255, s[86:87]
	ds_read_b128 v[232:235], v205 offset:63488
	ds_read_b128 v[236:239], v209 offset:14336
	s_waitcnt lgkmcnt(2)
	ds_read_b128 v[248:251], v209 offset:16384
	v_mfma_f32_16x16x32_f16 v[114:117], v[146:149], v[240:243], v[38:41]
	s_add_i32 m0, s79, 0x0
	v_mfma_f32_16x16x32_f16 v[118:121], v[150:153], v[240:243], v[34:37]
	global_load_lds_dwordx4 v224, s[88:89]
	v_mfma_f32_16x16x32_f16 v[122:125], v[146:149], v[244:247], v[30:33]
	s_add_i32 m0, s79, 0x2000
	v_mfma_f32_16x16x32_f16 v[126:129], v[150:153], v[244:247], v[26:29]
	global_load_lds_dwordx4 v226, s[88:89]
	v_mov_b64_e32 v[80:81], v[4:5]
	v_mov_b64_e32 v[78:79], v[2:3]
	s_waitcnt lgkmcnt(1)
	v_mfma_f32_16x16x32_f16 v[130:133], v[146:149], v[232:235], v[22:25]
	v_mfma_f32_16x16x32_f16 v[134:137], v[150:153], v[232:235], v[18:21]
	v_mov_b64_e32 v[72:73], v[8:9]
	v_mov_b64_e32 v[70:71], v[6:7]
	v_mfma_f32_16x16x32_f16 v[138:141], v[146:149], v[236:239], v[14:17]
	v_mfma_f32_16x16x32_f16 v[142:145], v[150:153], v[236:239], v[10:13]
	s_cbranch_vccnz .LBB2_97
	s_branch .Lnine_2
.LBB2_95:
	s_and_b64 vcc, exec, s[0:1]
	s_waitcnt lgkmcnt(2)
	v_mfma_f32_16x16x32_f16 v[82:85], v[146:149], v[70:73], v[74:77]
	v_mfma_f32_16x16x32_f16 v[86:89], v[150:153], v[70:73], v[66:69]
	v_mfma_f32_16x16x32_f16 v[90:93], v[146:149], v[78:81], v[62:65]
	v_mfma_f32_16x16x32_f16 v[94:97], v[150:153], v[78:81], v[58:61]
	ds_read_b128 v[240:243], v205 offset:59392
	ds_read_b128 v[244:247], v205 offset:61440
	s_waitcnt lgkmcnt(2)
	v_mfma_f32_16x16x32_f16 v[98:101], v[146:149], v[232:235], v[54:57]
	v_mfma_f32_16x16x32_f16 v[102:105], v[150:153], v[232:235], v[50:53]
	v_mfma_f32_16x16x32_f16 v[106:109], v[146:149], v[236:239], v[46:49]
	v_mfma_f32_16x16x32_f16 v[110:113], v[150:153], v[236:239], v[42:45]
	ds_read_b128 v[232:235], v205 offset:63488
	ds_read_b128 v[236:239], v209 offset:14336
	s_waitcnt lgkmcnt(2)
	ds_read_b128 v[248:251], v209 offset:16384
	v_mfma_f32_16x16x32_f16 v[114:117], v[146:149], v[240:243], v[38:41]
	v_mfma_f32_16x16x32_f16 v[118:121], v[150:153], v[240:243], v[34:37]
	v_mfma_f32_16x16x32_f16 v[122:125], v[146:149], v[244:247], v[30:33]
	v_mfma_f32_16x16x32_f16 v[126:129], v[150:153], v[244:247], v[26:29]
	v_mov_b64_e32 v[80:81], v[4:5]
	v_mov_b64_e32 v[78:79], v[2:3]
	s_waitcnt lgkmcnt(1)
	v_mfma_f32_16x16x32_f16 v[130:133], v[146:149], v[232:235], v[22:25]
	v_mfma_f32_16x16x32_f16 v[134:137], v[150:153], v[232:235], v[18:21]
	v_mov_b64_e32 v[72:73], v[8:9]
	v_mov_b64_e32 v[70:71], v[6:7]
	v_mfma_f32_16x16x32_f16 v[138:141], v[146:149], v[236:239], v[14:17]
	v_mfma_f32_16x16x32_f16 v[142:145], v[150:153], v[236:239], v[10:13]
	s_cbranch_vccnz .LBB2_97
.Lnine_2:
	s_waitcnt lgkmcnt(0)
	v_mfma_f32_16x16x32_f16 v[70:73], v[146:149], v[248:251], v[6:9]
	v_mfma_f32_16x16x32_f16 v[78:81], v[150:153], v[248:251], v[2:5]
.LBB2_97:
	s_waitcnt lgkmcnt(0)
	v_add_u32_e32 v150, 0, v199
	ds_read_b128 v[146:149], v150 offset:51200
	ds_read_b128 v[150:153], v150 offset:53248
	ds_read_b128 v[162:165], v207 offset:51200
	ds_read_b128 v[166:169], v207 offset:53248
	ds_read_b128 v[232:235], v207 offset:55296
	ds_read_b128 v[236:239], v207 offset:57344
	ds_read_b128 v[240:243], v207 offset:59392
	ds_read_b128 v[244:247], v207 offset:61440
	s_and_b64 vcc, exec, s[0:1]
	s_waitcnt lgkmcnt(5)
	v_mfma_f32_16x16x32_f16 v[82:85], v[146:149], v[162:165], v[82:85]
	v_mfma_f32_16x16x32_f16 v[86:89], v[150:153], v[162:165], v[86:89]
	s_waitcnt lgkmcnt(4)
	v_mfma_f32_16x16x32_f16 v[90:93], v[146:149], v[166:169], v[90:93]
	v_mfma_f32_16x16x32_f16 v[94:97], v[150:153], v[166:169], v[94:97]
	s_waitcnt lgkmcnt(3)
	v_mfma_f32_16x16x32_f16 v[98:101], v[146:149], v[232:235], v[98:101]
	v_mfma_f32_16x16x32_f16 v[102:105], v[150:153], v[232:235], v[102:105]
	ds_read_b128 v[232:235], v207 offset:63488
	s_waitcnt lgkmcnt(3)
	v_mfma_f32_16x16x32_f16 v[106:109], v[146:149], v[236:239], v[106:109]
	v_mfma_f32_16x16x32_f16 v[110:113], v[150:153], v[236:239], v[110:113]
	ds_read_b128 v[236:239], v211 offset:14336
	s_waitcnt lgkmcnt(3)
	ds_read_b128 v[248:251], v211 offset:16384
	v_mfma_f32_16x16x32_f16 v[114:117], v[146:149], v[240:243], v[114:117]
	v_mfma_f32_16x16x32_f16 v[118:121], v[150:153], v[240:243], v[118:121]
	s_waitcnt lgkmcnt(3)
	v_mfma_f32_16x16x32_f16 v[122:125], v[146:149], v[244:247], v[122:125]
	v_mfma_f32_16x16x32_f16 v[126:129], v[150:153], v[244:247], v[126:129]
	s_waitcnt lgkmcnt(2)
	v_mfma_f32_16x16x32_f16 v[130:133], v[146:149], v[232:235], v[130:133]
	v_mfma_f32_16x16x32_f16 v[134:137], v[150:153], v[232:235], v[134:137]
	s_waitcnt lgkmcnt(1)
	v_mfma_f32_16x16x32_f16 v[138:141], v[146:149], v[236:239], v[138:141]
	v_mfma_f32_16x16x32_f16 v[142:145], v[150:153], v[236:239], v[142:145]
	s_cbranch_vccnz .LBB2_108
	s_waitcnt lgkmcnt(0)
	v_mfma_f32_16x16x32_f16 v[70:73], v[146:149], v[248:251], v[70:73]
	v_mfma_f32_16x16x32_f16 v[78:81], v[150:153], v[248:251], v[78:81]
	s_cmpk_lg_i32 s6, 0x680
	s_mov_b64 s[30:31], -1
	s_cbranch_scc1 .LBB2_109

.Lil_3:
	s_and_b64 vcc, exec, s[0:1]
	s_waitcnt lgkmcnt(5)
	v_mfma_f32_16x16x32_f16 v[86:89], v[182:185], v[146:149], v[86:89]
	s_add_i32 m0, s79, 0x11000
	v_mfma_f32_16x16x32_f16 v[82:85], v[178:181], v[146:149], v[82:85]
	global_load_lds_dwordx4 v252, s[86:87]
	s_waitcnt lgkmcnt(4)
	v_mfma_f32_16x16x32_f16 v[90:93], v[178:181], v[150:153], v[90:93]
	s_add_i32 m0, s79, 0x13000
	v_mfma_f32_16x16x32_f16 v[94:97], v[182:185], v[150:153], v[94:97]
	global_load_lds_dwordx4 v253, s[86:87]
	s_waitcnt lgkmcnt(2)
	v_mfma_f32_16x16x32_f16 v[106:109], v[178:181], v[236:239], v[106:109]
	s_add_i32 m0, s79, 0x15000
	v_mfma_f32_16x16x32_f16 v[110:113], v[182:185], v[236:239], v[110:113]
	global_load_lds_dwordx4 v254, s[86:87]
	v_mfma_f32_16x16x32_f16 v[98:101], v[178:181], v[232:235], v[98:101]
	s_add_i32 m0, s79, 0x17000
	v_mfma_f32_16x16x32_f16 v[102:105], v[182:185], v[232:235], v[102:105]
	global_load_lds_dwordx4 v255, s[86:87]
	ds_read_b128 v[232:235], v213 offset:12288
	ds_read_b128 v[236:239], v213 offset:14336
	s_waitcnt lgkmcnt(3)
	ds_read_b128 v[248:251], v213 offset:16384
	v_mfma_f32_16x16x32_f16 v[146:149], v[178:181], v[240:243], v[114:117]
	s_add_i32 m0, s79, 0xc800
	v_mfma_f32_16x16x32_f16 v[150:153], v[182:185], v[240:243], v[118:121]
	global_load_lds_dwordx4 v224, s[88:89]
	s_waitcnt lgkmcnt(3)
	v_mfma_f32_16x16x32_f16 v[154:157], v[178:181], v[244:247], v[122:125]
	s_add_i32 m0, s79, 0xe800
	v_mfma_f32_16x16x32_f16 v[158:161], v[182:185], v[244:247], v[126:129]
	global_load_lds_dwordx4 v226, s[88:89]
	s_waitcnt lgkmcnt(2)
	v_mfma_f32_16x16x32_f16 v[162:165], v[178:181], v[232:235], v[130:133]
	v_mfma_f32_16x16x32_f16 v[166:169], v[182:185], v[232:235], v[134:137]
	s_waitcnt lgkmcnt(1)
	v_mfma_f32_16x16x32_f16 v[170:173], v[178:181], v[236:239], v[138:141]
	v_mfma_f32_16x16x32_f16 v[174:177], v[182:185], v[236:239], v[142:145]
	s_cbranch_vccnz .LBB2_106
	s_branch .Lnine_3
.LBB2_104:
	s_and_b64 vcc, exec, s[0:1]
	s_waitcnt lgkmcnt(5)
	v_mfma_f32_16x16x32_f16 v[86:89], v[182:185], v[146:149], v[86:89]
	v_mfma_f32_16x16x32_f16 v[82:85], v[178:181], v[146:149], v[82:85]
	s_waitcnt lgkmcnt(4)
	v_mfma_f32_16x16x32_f16 v[90:93], v[178:181], v[150:153], v[90:93]
	v_mfma_f32_16x16x32_f16 v[94:97], v[182:185], v[150:153], v[94:97]
	s_waitcnt lgkmcnt(2)
	v_mfma_f32_16x16x32_f16 v[106:109], v[178:181], v[236:239], v[106:109]
	v_mfma_f32_16x16x32_f16 v[110:113], v[182:185], v[236:239], v[110:113]
	v_mfma_f32_16x16x32_f16 v[98:101], v[178:181], v[232:235], v[98:101]
	v_mfma_f32_16x16x32_f16 v[102:105], v[182:185], v[232:235], v[102:105]
	ds_read_b128 v[232:235], v213 offset:12288
	ds_read_b128 v[236:239], v213 offset:14336
	s_waitcnt lgkmcnt(3)
	ds_read_b128 v[248:251], v213 offset:16384
	v_mfma_f32_16x16x32_f16 v[146:149], v[178:181], v[240:243], v[114:117]
	v_mfma_f32_16x16x32_f16 v[150:153], v[182:185], v[240:243], v[118:121]
	s_waitcnt lgkmcnt(3)
	v_mfma_f32_16x16x32_f16 v[154:157], v[178:181], v[244:247], v[122:125]
	v_mfma_f32_16x16x32_f16 v[158:161], v[182:185], v[244:247], v[126:129]
	s_waitcnt lgkmcnt(2)
	v_mfma_f32_16x16x32_f16 v[162:165], v[178:181], v[232:235], v[130:133]
	v_mfma_f32_16x16x32_f16 v[166:169], v[182:185], v[232:235], v[134:137]
	s_waitcnt lgkmcnt(1)
	v_mfma_f32_16x16x32_f16 v[170:173], v[178:181], v[236:239], v[138:141]
	v_mfma_f32_16x16x32_f16 v[174:177], v[182:185], v[236:239], v[142:145]
	s_cbranch_vccnz .LBB2_106
.Lnine_3:
	s_waitcnt lgkmcnt(0)
	v_mfma_f32_16x16x32_f16 v[70:73], v[178:181], v[248:251], v[70:73]
	v_mfma_f32_16x16x32_f16 v[78:81], v[182:185], v[248:251], v[78:81]
.LBB2_106:
	s_waitcnt lgkmcnt(0)
	v_add_u32_e32 v114, s37, v199
	ds_read_b128 v[178:181], v114
	ds_read_b128 v[182:185], v114 offset:2048
	v_add_u32_e32 v213, s37, v197
	ds_read_b128 v[114:117], v213
	ds_read_b128 v[118:121], v213 offset:2048
	ds_read_b128 v[232:235], v213 offset:4096
	ds_read_b128 v[236:239], v213 offset:6144
	ds_read_b128 v[240:243], v213 offset:8192
	ds_read_b128 v[244:247], v213 offset:10240
	s_and_b64 vcc, exec, s[0:1]
	s_waitcnt lgkmcnt(5)
	v_mfma_f32_16x16x32_f16 v[134:137], v[182:185], v[114:117], v[86:89]
	v_mfma_f32_16x16x32_f16 v[138:141], v[178:181], v[114:117], v[82:85]
	s_waitcnt lgkmcnt(4)
	v_mfma_f32_16x16x32_f16 v[130:133], v[178:181], v[118:121], v[90:93]
	v_mfma_f32_16x16x32_f16 v[126:129], v[182:185], v[118:121], v[94:97]
	s_waitcnt lgkmcnt(3)
	v_mfma_f32_16x16x32_f16 v[122:125], v[178:181], v[232:235], v[98:101]
	v_mfma_f32_16x16x32_f16 v[118:121], v[182:185], v[232:235], v[102:105]
	ds_read_b128 v[232:235], v213 offset:12288
	s_waitcnt lgkmcnt(3)
	v_mfma_f32_16x16x32_f16 v[114:117], v[178:181], v[236:239], v[106:109]
	v_mfma_f32_16x16x32_f16 v[110:113], v[182:185], v[236:239], v[110:113]
	ds_read_b128 v[236:239], v213 offset:14336
	s_waitcnt lgkmcnt(3)
	ds_read_b128 v[248:251], v213 offset:16384
	v_mfma_f32_16x16x32_f16 v[106:109], v[178:181], v[240:243], v[146:149]
	v_mfma_f32_16x16x32_f16 v[102:105], v[182:185], v[240:243], v[150:153]
	s_waitcnt lgkmcnt(3)
	v_mfma_f32_16x16x32_f16 v[98:101], v[178:181], v[244:247], v[154:157]
	v_mfma_f32_16x16x32_f16 v[94:97], v[182:185], v[244:247], v[158:161]
	s_waitcnt lgkmcnt(2)
	v_mfma_f32_16x16x32_f16 v[90:93], v[178:181], v[232:235], v[162:165]
	v_mfma_f32_16x16x32_f16 v[86:89], v[182:185], v[232:235], v[166:169]
	s_waitcnt lgkmcnt(1)
	v_mfma_f32_16x16x32_f16 v[142:145], v[178:181], v[236:239], v[170:173]
	v_mfma_f32_16x16x32_f16 v[82:85], v[182:185], v[236:239], v[174:177]
	s_cbranch_vccnz .LBB2_66
	s_waitcnt lgkmcnt(0)
	v_mfma_f32_16x16x32_f16 v[70:73], v[178:181], v[248:251], v[70:73]
	v_mfma_f32_16x16x32_f16 v[78:81], v[182:185], v[248:251], v[78:81]
	s_branch .LBB2_66

.LBB3_76:
	v_bitop3_b32 v62, v135, v62, 4 bitop3:0x36
	v_lshlrev_b32_e32 v117, 4, v62
	v_add_u32_e32 v62, v63, v117
	v_add_u32_e32 v123, 0, v62
	ds_read_b128 v[86:89], v123 offset:20480
	v_or_b32_e32 v114, v117, v115
	v_add_u32_e32 v137, 0, v114
	ds_read_b128 v[90:93], v123 offset:22528
	ds_read_b128 v[62:65], v137
	ds_read_b128 v[118:121], v137 offset:2048
	s_waitcnt lgkmcnt(0)
	v_mfma_f32_16x16x32_f16 v[22:25], v[90:93], v[62:65], v[22:25]
	s_andn2_b64 vcc, exec, s[8:9]
	v_mfma_f32_16x16x32_f16 v[18:21], v[86:89], v[62:65], v[18:21]
	v_mfma_f32_16x16x32_f16 v[26:29], v[86:89], v[118:121], v[26:29]
	v_mfma_f32_16x16x32_f16 v[30:33], v[90:93], v[118:121], v[30:33]
	ds_read_b128 v[62:65], v137 offset:4096
	ds_read_b128 v[118:121], v137 offset:6144
	s_waitcnt lgkmcnt(0)
	v_mfma_f32_16x16x32_f16 v[34:37], v[86:89], v[62:65], v[34:37]
	v_mfma_f32_16x16x32_f16 v[38:41], v[90:93], v[62:65], v[38:41]
	v_mfma_f32_16x16x32_f16 v[42:45], v[86:89], v[118:121], v[42:45]
	v_mfma_f32_16x16x32_f16 v[46:49], v[90:93], v[118:121], v[46:49]
	ds_read_b128 v[62:65], v137 offset:8192
	ds_read_b128 v[118:121], v137 offset:10240
	s_waitcnt lgkmcnt(0)
	ds_read_b128 v[176:179], v137 offset:16384
	v_mfma_f32_16x16x32_f16 v[50:53], v[86:89], v[62:65], v[50:53]
	v_mfma_f32_16x16x32_f16 v[54:57], v[90:93], v[62:65], v[54:57]
	v_mfma_f32_16x16x32_f16 v[62:65], v[86:89], v[118:121], v[58:61]
	v_mfma_f32_16x16x32_f16 v[58:61], v[90:93], v[118:121], v[70:73]
	s_nop 2
	ds_read_b128 v[70:73], v137 offset:12288
	ds_read_b128 v[118:121], v137 offset:14336
	s_waitcnt lgkmcnt(0)
	v_mfma_f32_16x16x32_f16 v[66:69], v[86:89], v[70:73], v[66:69]
	v_mfma_f32_16x16x32_f16 v[70:73], v[90:93], v[70:73], v[74:77]
	v_mfma_f32_16x16x32_f16 v[74:77], v[86:89], v[118:121], v[78:81]
	s_nop 2
	v_cndmask_b32_e64 v78, 0, 1, s[8:9]
	v_cmp_ne_u32_e64 s[4:5], 1, v78
	v_mfma_f32_16x16x32_f16 v[78:81], v[90:93], v[118:121], v[82:85]
	s_cbranch_vccz .LBB3_176
	s_nop 1
	v_cndmask_b32_e64 v82, 0, 1, s[12:13]
	v_cmp_ne_u32_e64 s[6:7], 1, v82
	s_andn2_b64 vcc, exec, s[12:13]
	s_cbranch_vccz .LBB3_177

.LBB3_83:
	v_add_u32_e32 v82, s18, v115
	v_add_u32_e32 v118, 0x5000, v82
	v_or_b32_e32 v115, v118, v116
	v_add_u32_e32 v124, 0, v115
	ds_read_b128 v[86:89], v124 offset:53248
	ds_read_b128 v[90:93], v124 offset:55296
	ds_read_b128 v[82:85], v136 offset:53248
	ds_read_b128 v[138:141], v136 offset:55296
	s_and_b64 vcc, exec, s[4:5]
	s_waitcnt lgkmcnt(0)
	v_mfma_f32_16x16x32_f16 v[18:21], v[86:89], v[82:85], v[18:21]
	s_mov_b32 m0, s76
	v_mfma_f32_16x16x32_f16 v[22:25], v[90:93], v[82:85], v[22:25]
	global_load_lds_dwordx4 v168, s[72:73]
	v_mfma_f32_16x16x32_f16 v[26:29], v[86:89], v[138:141], v[26:29]
	s_mov_b32 m0, s77
	v_mfma_f32_16x16x32_f16 v[30:33], v[90:93], v[138:141], v[30:33]
	global_load_lds_dwordx4 v169, s[72:73]
	ds_read_b128 v[82:85], v136 offset:57344
	ds_read_b128 v[138:141], v136 offset:59392
	s_waitcnt lgkmcnt(0)
	v_mfma_f32_16x16x32_f16 v[34:37], v[86:89], v[82:85], v[34:37]
	s_mov_b32 m0, s78
	v_mfma_f32_16x16x32_f16 v[38:41], v[90:93], v[82:85], v[38:41]
	global_load_lds_dwordx4 v170, s[72:73]
	v_mfma_f32_16x16x32_f16 v[42:45], v[86:89], v[138:141], v[42:45]
	s_mov_b32 m0, s79
	v_mfma_f32_16x16x32_f16 v[46:49], v[90:93], v[138:141], v[46:49]
	global_load_lds_dwordx4 v171, s[72:73]
	ds_read_b128 v[82:85], v136 offset:61440
	ds_read_b128 v[140:143], v136 offset:63488
	v_add_u32_e32 v138, 0xd000, v136
	s_waitcnt lgkmcnt(0)
	ds_read_b128 v[176:179], v138 offset:16384
	v_mfma_f32_16x16x32_f16 v[50:53], v[86:89], v[82:85], v[50:53]
	s_mov_b32 m0, s80
	v_mfma_f32_16x16x32_f16 v[54:57], v[90:93], v[82:85], v[54:57]
	global_load_lds_dwordx4 v172, s[74:75]
	v_mfma_f32_16x16x32_f16 v[62:65], v[86:89], v[140:143], v[62:65]
	s_mov_b32 m0, s81
	v_mfma_f32_16x16x32_f16 v[82:85], v[90:93], v[140:143], v[58:61]
	global_load_lds_dwordx4 v173, s[74:75]
	s_nop 2
	ds_read_b128 v[58:61], v138 offset:12288
	ds_read_b128 v[140:143], v138 offset:14336
	s_waitcnt lgkmcnt(0)
	v_mfma_f32_16x16x32_f16 v[66:69], v[86:89], v[58:61], v[66:69]
	v_mfma_f32_16x16x32_f16 v[70:73], v[90:93], v[58:61], v[70:73]
	v_mfma_f32_16x16x32_f16 v[74:77], v[86:89], v[140:143], v[74:77]
	v_mfma_f32_16x16x32_f16 v[78:81], v[90:93], v[140:143], v[78:81]
	s_cbranch_vccnz .LBB3_85
	s_waitcnt lgkmcnt(0)
	v_mfma_f32_16x16x32_f16 v[10:13], v[86:89], v[176:179], v[10:13]
	v_mfma_f32_16x16x32_f16 v[14:17], v[90:93], v[176:179], v[14:17]

.LBB3_87:
	v_or_b32_e32 v116, v118, v117
	v_add_u32_e32 v140, 0, v116
	ds_read_b128 v[86:89], v140 offset:53248
	ds_read_b128 v[90:93], v140 offset:55296
	ds_read_b128 v[58:61], v137 offset:53248
	ds_read_b128 v[118:121], v137 offset:55296
	v_add_u32_e32 v139, 0xd000, v137
	s_and_b64 vcc, exec, s[4:5]
	s_waitcnt lgkmcnt(0)
	v_mfma_f32_16x16x32_f16 v[18:21], v[86:89], v[58:61], v[18:21]
	v_mfma_f32_16x16x32_f16 v[22:25], v[90:93], v[58:61], v[22:25]
	v_mfma_f32_16x16x32_f16 v[26:29], v[86:89], v[118:121], v[26:29]
	v_mfma_f32_16x16x32_f16 v[30:33], v[90:93], v[118:121], v[30:33]
	ds_read_b128 v[58:61], v137 offset:57344
	ds_read_b128 v[118:121], v137 offset:59392
	s_waitcnt lgkmcnt(0)
	v_mfma_f32_16x16x32_f16 v[34:37], v[86:89], v[58:61], v[34:37]
	v_mfma_f32_16x16x32_f16 v[38:41], v[90:93], v[58:61], v[38:41]
	v_mfma_f32_16x16x32_f16 v[42:45], v[86:89], v[118:121], v[42:45]
	v_mfma_f32_16x16x32_f16 v[46:49], v[90:93], v[118:121], v[46:49]
	ds_read_b128 v[58:61], v137 offset:61440
	ds_read_b128 v[118:121], v137 offset:63488
	s_waitcnt lgkmcnt(0)
	ds_read_b128 v[176:179], v139 offset:16384
	v_mfma_f32_16x16x32_f16 v[50:53], v[86:89], v[58:61], v[50:53]
	v_mfma_f32_16x16x32_f16 v[54:57], v[90:93], v[58:61], v[54:57]
	v_mfma_f32_16x16x32_f16 v[58:61], v[86:89], v[118:121], v[62:65]
	v_mfma_f32_16x16x32_f16 v[62:65], v[90:93], v[118:121], v[82:85]
	s_nop 2
	ds_read_b128 v[82:85], v139 offset:12288
	ds_read_b128 v[118:121], v139 offset:14336
	s_waitcnt lgkmcnt(0)
	v_mfma_f32_16x16x32_f16 v[66:69], v[86:89], v[82:85], v[66:69]
	v_mfma_f32_16x16x32_f16 v[70:73], v[90:93], v[82:85], v[70:73]
	v_mfma_f32_16x16x32_f16 v[74:77], v[86:89], v[118:121], v[74:77]
	v_mfma_f32_16x16x32_f16 v[78:81], v[90:93], v[118:121], v[78:81]
	s_cbranch_vccz .LBB3_179
	s_and_b64 vcc, exec, s[6:7]
	s_cbranch_vccz .LBB3_180

.LBB3_94:
	s_and_b64 vcc, exec, s[4:5]
	s_waitcnt lgkmcnt(5)
	v_mfma_f32_16x16x32_f16 v[22:25], v[86:89], v[118:121], v[22:25]
	s_mov_b32 m0, s82
	v_mfma_f32_16x16x32_f16 v[18:21], v[82:85], v[118:121], v[18:21]
	global_load_lds_dwordx4 v168, s[72:73]
	s_waitcnt lgkmcnt(4)
	v_mfma_f32_16x16x32_f16 v[26:29], v[82:85], v[142:145], v[26:29]
	s_mov_b32 m0, s83
	v_mfma_f32_16x16x32_f16 v[30:33], v[86:89], v[142:145], v[30:33]
	global_load_lds_dwordx4 v169, s[72:73]
	s_waitcnt lgkmcnt(3)
	v_mfma_f32_16x16x32_f16 v[34:37], v[82:85], v[148:151], v[34:37]
	s_mov_b32 m0, s84
	v_mfma_f32_16x16x32_f16 v[38:41], v[86:89], v[148:151], v[38:41]
	global_load_lds_dwordx4 v170, s[72:73]
	ds_read_b128 v[148:151], v125 offset:12288
	s_waitcnt lgkmcnt(3)
	v_mfma_f32_16x16x32_f16 v[42:45], v[82:85], v[152:155], v[42:45]
	s_mov_b32 m0, s85
	v_mfma_f32_16x16x32_f16 v[46:49], v[86:89], v[152:155], v[46:49]
	global_load_lds_dwordx4 v171, s[72:73]
	ds_read_b128 v[152:155], v125 offset:14336
	s_waitcnt lgkmcnt(3)
	ds_read_b128 v[176:179], v125 offset:16384
	v_mfma_f32_16x16x32_f16 v[50:53], v[82:85], v[156:159], v[50:53]
	s_mov_b32 m0, s86
	v_mfma_f32_16x16x32_f16 v[54:57], v[86:89], v[156:159], v[54:57]
	global_load_lds_dwordx4 v172, s[74:75]
	s_waitcnt lgkmcnt(3)
	v_mfma_f32_16x16x32_f16 v[58:61], v[82:85], v[160:163], v[58:61]
	s_mov_b32 m0, s87
	v_mfma_f32_16x16x32_f16 v[62:65], v[86:89], v[160:163], v[62:65]
	global_load_lds_dwordx4 v173, s[74:75]
	s_waitcnt lgkmcnt(2)
	v_mfma_f32_16x16x32_f16 v[66:69], v[82:85], v[148:151], v[66:69]
	v_mfma_f32_16x16x32_f16 v[70:73], v[86:89], v[148:151], v[70:73]
	s_waitcnt lgkmcnt(1)
	v_mfma_f32_16x16x32_f16 v[74:77], v[82:85], v[152:155], v[74:77]
	v_mfma_f32_16x16x32_f16 v[78:81], v[86:89], v[152:155], v[78:81]
	s_cbranch_vccnz .LBB3_96
	s_waitcnt lgkmcnt(0)
	v_mfma_f32_16x16x32_f16 v[10:13], v[82:85], v[176:179], v[10:13]
	v_mfma_f32_16x16x32_f16 v[14:17], v[86:89], v[176:179], v[14:17]

.LBB3_98:
	s_waitcnt lgkmcnt(0)
	v_add_u32_e32 v142, s17, v116
	ds_read_b128 v[82:85], v142
	ds_read_b128 v[86:89], v142 offset:2048
	v_add_u32_e32 v141, s17, v114
	ds_read_b128 v[114:117], v141
	ds_read_b128 v[118:121], v141 offset:2048
	ds_read_b128 v[148:151], v141 offset:4096
	ds_read_b128 v[152:155], v141 offset:6144
	ds_read_b128 v[156:159], v141 offset:8192
	ds_read_b128 v[160:163], v141 offset:10240
	s_and_b64 vcc, exec, s[4:5]
	s_waitcnt lgkmcnt(5)
	v_mfma_f32_16x16x32_f16 v[22:25], v[86:89], v[114:117], v[22:25]
	v_mfma_f32_16x16x32_f16 v[18:21], v[82:85], v[114:117], v[18:21]
	s_waitcnt lgkmcnt(4)
	v_mfma_f32_16x16x32_f16 v[26:29], v[82:85], v[118:121], v[26:29]
	v_mfma_f32_16x16x32_f16 v[30:33], v[86:89], v[118:121], v[30:33]
	s_waitcnt lgkmcnt(3)
	v_mfma_f32_16x16x32_f16 v[34:37], v[82:85], v[148:151], v[34:37]
	v_mfma_f32_16x16x32_f16 v[38:41], v[86:89], v[148:151], v[38:41]
	ds_read_b128 v[148:151], v141 offset:12288
	s_waitcnt lgkmcnt(3)
	v_mfma_f32_16x16x32_f16 v[42:45], v[82:85], v[152:155], v[42:45]
	v_mfma_f32_16x16x32_f16 v[46:49], v[86:89], v[152:155], v[46:49]
	ds_read_b128 v[152:155], v141 offset:14336
	s_waitcnt lgkmcnt(3)
	ds_read_b128 v[176:179], v141 offset:16384
	v_mfma_f32_16x16x32_f16 v[50:53], v[82:85], v[156:159], v[50:53]
	v_mfma_f32_16x16x32_f16 v[54:57], v[86:89], v[156:159], v[54:57]
	s_waitcnt lgkmcnt(3)
	v_mfma_f32_16x16x32_f16 v[58:61], v[82:85], v[160:163], v[58:61]
	v_mfma_f32_16x16x32_f16 v[62:65], v[86:89], v[160:163], v[62:65]
	s_waitcnt lgkmcnt(2)
	v_mfma_f32_16x16x32_f16 v[66:69], v[82:85], v[148:151], v[66:69]
	v_mfma_f32_16x16x32_f16 v[70:73], v[86:89], v[148:151], v[70:73]
	s_waitcnt lgkmcnt(1)
	v_mfma_f32_16x16x32_f16 v[74:77], v[82:85], v[152:155], v[74:77]
	v_mfma_f32_16x16x32_f16 v[78:81], v[86:89], v[152:155], v[78:81]
	s_cbranch_vccnz .LBB3_100
	s_waitcnt lgkmcnt(0)
	v_mfma_f32_16x16x32_f16 v[10:13], v[82:85], v[176:179], v[10:13]
	v_mfma_f32_16x16x32_f16 v[14:17], v[86:89], v[176:179], v[14:17]

.LBB3_108:
	s_waitcnt lgkmcnt(0)
	ds_read_b128 v[82:85], v122 offset:20480
	ds_read_b128 v[86:89], v122 offset:22528
	ds_read_b128 v[112:115], v136
	ds_read_b128 v[116:119], v136 offset:2048
	ds_read_b128 v[148:151], v136 offset:4096
	ds_read_b128 v[152:155], v136 offset:6144
	ds_read_b128 v[156:159], v136 offset:8192
	ds_read_b128 v[160:163], v136 offset:10240
	s_and_b64 vcc, exec, s[4:5]
	s_waitcnt lgkmcnt(5)
	v_mfma_f32_16x16x32_f16 v[18:21], v[82:85], v[112:115], v[18:21]
	s_mov_b32 m0, s88
	v_mfma_f32_16x16x32_f16 v[22:25], v[86:89], v[112:115], v[22:25]
	global_load_lds_dwordx4 v168, s[72:73]
	s_waitcnt lgkmcnt(4)
	v_mfma_f32_16x16x32_f16 v[26:29], v[82:85], v[116:119], v[26:29]
	s_mov_b32 m0, s89
	v_mfma_f32_16x16x32_f16 v[30:33], v[86:89], v[116:119], v[30:33]
	global_load_lds_dwordx4 v169, s[72:73]
	s_waitcnt lgkmcnt(3)
	v_mfma_f32_16x16x32_f16 v[34:37], v[82:85], v[148:151], v[34:37]
	s_mov_b32 m0, s90
	v_mfma_f32_16x16x32_f16 v[38:41], v[86:89], v[148:151], v[38:41]
	global_load_lds_dwordx4 v170, s[72:73]
	ds_read_b128 v[148:151], v136 offset:12288
	s_waitcnt lgkmcnt(3)
	v_mfma_f32_16x16x32_f16 v[42:45], v[82:85], v[152:155], v[42:45]
	s_mov_b32 m0, s91
	v_mfma_f32_16x16x32_f16 v[46:49], v[86:89], v[152:155], v[46:49]
	global_load_lds_dwordx4 v171, s[72:73]
	ds_read_b128 v[152:155], v136 offset:14336
	s_waitcnt lgkmcnt(3)
	ds_read_b128 v[176:179], v136 offset:16384
	v_mfma_f32_16x16x32_f16 v[50:53], v[82:85], v[156:159], v[50:53]
	s_mov_b32 m0, s92
	v_mfma_f32_16x16x32_f16 v[54:57], v[86:89], v[156:159], v[54:57]
	global_load_lds_dwordx4 v172, s[74:75]
	s_waitcnt lgkmcnt(3)
	v_mfma_f32_16x16x32_f16 v[58:61], v[82:85], v[160:163], v[58:61]
	s_mov_b32 m0, s93
	v_mfma_f32_16x16x32_f16 v[62:65], v[86:89], v[160:163], v[62:65]
	global_load_lds_dwordx4 v173, s[74:75]
	s_waitcnt lgkmcnt(2)
	v_mfma_f32_16x16x32_f16 v[66:69], v[82:85], v[148:151], v[66:69]
	v_mfma_f32_16x16x32_f16 v[70:73], v[86:89], v[148:151], v[70:73]
	s_waitcnt lgkmcnt(1)
	v_mfma_f32_16x16x32_f16 v[74:77], v[82:85], v[152:155], v[74:77]
	v_mfma_f32_16x16x32_f16 v[78:81], v[86:89], v[152:155], v[78:81]
	s_cbranch_vccnz .LBB3_110
	s_waitcnt lgkmcnt(0)
	v_mfma_f32_16x16x32_f16 v[10:13], v[82:85], v[176:179], v[10:13]
	v_mfma_f32_16x16x32_f16 v[14:17], v[86:89], v[176:179], v[14:17]

.LBB3_112:
	s_waitcnt lgkmcnt(0)
	ds_read_b128 v[82:85], v123 offset:20480
	ds_read_b128 v[86:89], v123 offset:22528
	ds_read_b128 v[112:115], v137
	ds_read_b128 v[116:119], v137 offset:2048
	ds_read_b128 v[148:151], v137 offset:4096
	ds_read_b128 v[152:155], v137 offset:6144
	ds_read_b128 v[156:159], v137 offset:8192
	ds_read_b128 v[160:163], v137 offset:10240
	s_and_b64 vcc, exec, s[4:5]
	s_waitcnt lgkmcnt(5)
	v_mfma_f32_16x16x32_f16 v[18:21], v[82:85], v[112:115], v[18:21]
	v_mfma_f32_16x16x32_f16 v[22:25], v[86:89], v[112:115], v[22:25]
	s_waitcnt lgkmcnt(4)
	v_mfma_f32_16x16x32_f16 v[26:29], v[82:85], v[116:119], v[26:29]
	v_mfma_f32_16x16x32_f16 v[30:33], v[86:89], v[116:119], v[30:33]
	s_waitcnt lgkmcnt(3)
	v_mfma_f32_16x16x32_f16 v[34:37], v[82:85], v[148:151], v[34:37]
	v_mfma_f32_16x16x32_f16 v[38:41], v[86:89], v[148:151], v[38:41]
	ds_read_b128 v[148:151], v137 offset:12288
	s_waitcnt lgkmcnt(3)
	v_mfma_f32_16x16x32_f16 v[42:45], v[82:85], v[152:155], v[42:45]
	v_mfma_f32_16x16x32_f16 v[46:49], v[86:89], v[152:155], v[46:49]
	ds_read_b128 v[152:155], v137 offset:14336
	s_waitcnt lgkmcnt(3)
	ds_read_b128 v[176:179], v137 offset:16384
	v_mfma_f32_16x16x32_f16 v[50:53], v[82:85], v[156:159], v[50:53]
	v_mfma_f32_16x16x32_f16 v[54:57], v[86:89], v[156:159], v[54:57]
	s_waitcnt lgkmcnt(3)
	v_mfma_f32_16x16x32_f16 v[58:61], v[82:85], v[160:163], v[58:61]
	v_mfma_f32_16x16x32_f16 v[62:65], v[86:89], v[160:163], v[62:65]
	s_waitcnt lgkmcnt(2)
	v_mfma_f32_16x16x32_f16 v[66:69], v[82:85], v[148:151], v[66:69]
	v_mfma_f32_16x16x32_f16 v[70:73], v[86:89], v[148:151], v[70:73]
	s_waitcnt lgkmcnt(1)
	v_mfma_f32_16x16x32_f16 v[74:77], v[82:85], v[152:155], v[74:77]
	v_mfma_f32_16x16x32_f16 v[78:81], v[86:89], v[152:155], v[78:81]
	s_cbranch_vccz .LBB3_182
	s_and_b64 vcc, exec, s[6:7]
	s_cbranch_vccz .LBB3_183

.LBB3_119:
	s_and_b64 vcc, exec, s[4:5]
	s_waitcnt lgkmcnt(5)
	v_mfma_f32_16x16x32_f16 v[18:21], v[82:85], v[112:115], v[18:21]
	s_mov_b32 m0, s76
	v_mfma_f32_16x16x32_f16 v[22:25], v[86:89], v[112:115], v[22:25]
	global_load_lds_dwordx4 v168, s[72:73]
	s_waitcnt lgkmcnt(4)
	v_mfma_f32_16x16x32_f16 v[26:29], v[82:85], v[116:119], v[26:29]
	s_mov_b32 m0, s77
	v_mfma_f32_16x16x32_f16 v[30:33], v[86:89], v[116:119], v[30:33]
	global_load_lds_dwordx4 v169, s[72:73]
	s_waitcnt lgkmcnt(3)
	v_mfma_f32_16x16x32_f16 v[34:37], v[82:85], v[148:151], v[34:37]
	s_mov_b32 m0, s78
	v_mfma_f32_16x16x32_f16 v[38:41], v[86:89], v[148:151], v[38:41]
	global_load_lds_dwordx4 v170, s[72:73]
	ds_read_b128 v[148:151], v138 offset:12288
	s_waitcnt lgkmcnt(3)
	v_mfma_f32_16x16x32_f16 v[42:45], v[82:85], v[152:155], v[42:45]
	s_mov_b32 m0, s79
	v_mfma_f32_16x16x32_f16 v[46:49], v[86:89], v[152:155], v[46:49]
	global_load_lds_dwordx4 v171, s[72:73]
	ds_read_b128 v[152:155], v138 offset:14336
	s_waitcnt lgkmcnt(3)
	ds_read_b128 v[176:179], v138 offset:16384
	v_mfma_f32_16x16x32_f16 v[50:53], v[82:85], v[156:159], v[50:53]
	s_mov_b32 m0, s80
	v_mfma_f32_16x16x32_f16 v[54:57], v[86:89], v[156:159], v[54:57]
	global_load_lds_dwordx4 v172, s[74:75]
	s_waitcnt lgkmcnt(3)
	v_mfma_f32_16x16x32_f16 v[58:61], v[82:85], v[160:163], v[58:61]
	s_mov_b32 m0, s81
	v_mfma_f32_16x16x32_f16 v[62:65], v[86:89], v[160:163], v[62:65]
	global_load_lds_dwordx4 v173, s[74:75]
	s_waitcnt lgkmcnt(2)
	v_mfma_f32_16x16x32_f16 v[66:69], v[82:85], v[148:151], v[66:69]
	v_mfma_f32_16x16x32_f16 v[70:73], v[86:89], v[148:151], v[70:73]
	s_waitcnt lgkmcnt(1)
	v_mfma_f32_16x16x32_f16 v[74:77], v[82:85], v[152:155], v[74:77]
	v_mfma_f32_16x16x32_f16 v[78:81], v[86:89], v[152:155], v[78:81]
	s_cbranch_vccnz .LBB3_121
	s_waitcnt lgkmcnt(0)
	v_mfma_f32_16x16x32_f16 v[10:13], v[82:85], v[176:179], v[10:13]
	v_mfma_f32_16x16x32_f16 v[14:17], v[86:89], v[176:179], v[14:17]

.LBB3_123:
	s_waitcnt lgkmcnt(0)
	ds_read_b128 v[82:85], v140 offset:53248
	ds_read_b128 v[86:89], v140 offset:55296
	ds_read_b128 v[112:115], v137 offset:53248
	ds_read_b128 v[116:119], v137 offset:55296
	ds_read_b128 v[148:151], v137 offset:57344
	ds_read_b128 v[152:155], v137 offset:59392
	ds_read_b128 v[156:159], v137 offset:61440
	ds_read_b128 v[160:163], v137 offset:63488
	s_and_b64 vcc, exec, s[4:5]
	s_waitcnt lgkmcnt(5)
	v_mfma_f32_16x16x32_f16 v[18:21], v[82:85], v[112:115], v[18:21]
	v_mfma_f32_16x16x32_f16 v[22:25], v[86:89], v[112:115], v[22:25]
	s_waitcnt lgkmcnt(4)
	v_mfma_f32_16x16x32_f16 v[26:29], v[82:85], v[116:119], v[26:29]
	v_mfma_f32_16x16x32_f16 v[30:33], v[86:89], v[116:119], v[30:33]
	s_waitcnt lgkmcnt(3)
	v_mfma_f32_16x16x32_f16 v[34:37], v[82:85], v[148:151], v[34:37]
	v_mfma_f32_16x16x32_f16 v[38:41], v[86:89], v[148:151], v[38:41]
	ds_read_b128 v[148:151], v139 offset:12288
	s_waitcnt lgkmcnt(3)
	v_mfma_f32_16x16x32_f16 v[42:45], v[82:85], v[152:155], v[42:45]
	v_mfma_f32_16x16x32_f16 v[46:49], v[86:89], v[152:155], v[46:49]
	ds_read_b128 v[152:155], v139 offset:14336
	s_waitcnt lgkmcnt(3)
	ds_read_b128 v[176:179], v139 offset:16384
	v_mfma_f32_16x16x32_f16 v[50:53], v[82:85], v[156:159], v[50:53]
	v_mfma_f32_16x16x32_f16 v[54:57], v[86:89], v[156:159], v[54:57]
	s_waitcnt lgkmcnt(3)
	v_mfma_f32_16x16x32_f16 v[58:61], v[82:85], v[160:163], v[58:61]
	v_mfma_f32_16x16x32_f16 v[62:65], v[86:89], v[160:163], v[62:65]
	s_waitcnt lgkmcnt(2)
	v_mfma_f32_16x16x32_f16 v[66:69], v[82:85], v[148:151], v[66:69]
	v_mfma_f32_16x16x32_f16 v[70:73], v[86:89], v[148:151], v[70:73]
	s_waitcnt lgkmcnt(1)
	v_mfma_f32_16x16x32_f16 v[74:77], v[82:85], v[152:155], v[74:77]
	v_mfma_f32_16x16x32_f16 v[78:81], v[86:89], v[152:155], v[78:81]
	s_cbranch_vccz .LBB3_185
	s_and_b64 vcc, exec, s[6:7]
	s_cbranch_vccz .LBB3_186

.LBB3_130:
	s_and_b64 vcc, exec, s[4:5]
	s_waitcnt lgkmcnt(5)
	v_mfma_f32_16x16x32_f16 v[18:21], v[114:117], v[82:85], v[18:21]
	s_mov_b32 m0, s82
	v_mfma_f32_16x16x32_f16 v[22:25], v[118:121], v[82:85], v[22:25]
	global_load_lds_dwordx4 v168, s[72:73]
	s_waitcnt lgkmcnt(4)
	v_mfma_f32_16x16x32_f16 v[26:29], v[114:117], v[86:89], v[26:29]
	s_mov_b32 m0, s83
	v_mfma_f32_16x16x32_f16 v[30:33], v[118:121], v[86:89], v[30:33]
	global_load_lds_dwordx4 v169, s[72:73]
	s_waitcnt lgkmcnt(2)
	v_mfma_f32_16x16x32_f16 v[42:45], v[114:117], v[152:155], v[42:45]
	s_mov_b32 m0, s84
	v_mfma_f32_16x16x32_f16 v[46:49], v[118:121], v[152:155], v[46:49]
	global_load_lds_dwordx4 v170, s[72:73]
	v_mfma_f32_16x16x32_f16 v[34:37], v[114:117], v[148:151], v[34:37]
	s_mov_b32 m0, s85
	v_mfma_f32_16x16x32_f16 v[38:41], v[118:121], v[148:151], v[38:41]
	global_load_lds_dwordx4 v171, s[72:73]
	ds_read_b128 v[148:151], v125 offset:12288
	ds_read_b128 v[152:155], v125 offset:14336
	s_waitcnt lgkmcnt(3)
	ds_read_b128 v[176:179], v125 offset:16384
	v_mfma_f32_16x16x32_f16 v[82:85], v[114:117], v[156:159], v[50:53]
	s_mov_b32 m0, s86
	v_mfma_f32_16x16x32_f16 v[86:89], v[118:121], v[156:159], v[54:57]
	global_load_lds_dwordx4 v172, s[74:75]
	s_nop 1
	s_waitcnt lgkmcnt(3)
	v_mfma_f32_16x16x32_f16 v[90:93], v[114:117], v[160:163], v[58:61]
	s_mov_b32 m0, s87
	v_mfma_f32_16x16x32_f16 v[94:97], v[118:121], v[160:163], v[62:65]
	global_load_lds_dwordx4 v173, s[74:75]
	s_waitcnt lgkmcnt(2)
	v_mfma_f32_16x16x32_f16 v[98:101], v[114:117], v[148:151], v[66:69]
	v_mfma_f32_16x16x32_f16 v[102:105], v[118:121], v[148:151], v[70:73]
	s_waitcnt lgkmcnt(1)
	v_mfma_f32_16x16x32_f16 v[106:109], v[114:117], v[152:155], v[74:77]
	v_mfma_f32_16x16x32_f16 v[110:113], v[118:121], v[152:155], v[78:81]
	s_cbranch_vccnz .LBB3_132
	s_waitcnt lgkmcnt(0)
	v_mfma_f32_16x16x32_f16 v[10:13], v[114:117], v[176:179], v[10:13]
	v_mfma_f32_16x16x32_f16 v[14:17], v[118:121], v[176:179], v[14:17]

.LBB3_134:
	s_waitcnt lgkmcnt(0)
	ds_read_b128 v[114:117], v142
	ds_read_b128 v[118:121], v142 offset:2048
	ds_read_b128 v[54:57], v141
	ds_read_b128 v[58:61], v141 offset:2048
	ds_read_b128 v[148:151], v141 offset:4096
	ds_read_b128 v[152:155], v141 offset:6144
	ds_read_b128 v[156:159], v141 offset:8192
	ds_read_b128 v[160:163], v141 offset:10240
	s_and_b64 vcc, exec, s[4:5]
	s_waitcnt lgkmcnt(5)
	v_mfma_f32_16x16x32_f16 v[50:53], v[114:117], v[54:57], v[18:21]
	v_mfma_f32_16x16x32_f16 v[54:57], v[118:121], v[54:57], v[22:25]
	s_waitcnt lgkmcnt(4)
	v_mfma_f32_16x16x32_f16 v[18:21], v[114:117], v[58:61], v[26:29]
	v_mfma_f32_16x16x32_f16 v[22:25], v[118:121], v[58:61], v[30:33]
	s_nop 1
	s_waitcnt lgkmcnt(3)
	v_mfma_f32_16x16x32_f16 v[58:61], v[114:117], v[148:151], v[34:37]
	v_mfma_f32_16x16x32_f16 v[62:65], v[118:121], v[148:151], v[38:41]
	ds_read_b128 v[148:151], v141 offset:12288
	s_nop 1
	s_waitcnt lgkmcnt(3)
	v_mfma_f32_16x16x32_f16 v[26:29], v[114:117], v[152:155], v[42:45]
	v_mfma_f32_16x16x32_f16 v[30:33], v[118:121], v[152:155], v[46:49]
	ds_read_b128 v[152:155], v141 offset:14336
	s_nop 1
	s_waitcnt lgkmcnt(3)
	ds_read_b128 v[176:179], v141 offset:16384
	v_mfma_f32_16x16x32_f16 v[66:69], v[114:117], v[156:159], v[82:85]
	v_mfma_f32_16x16x32_f16 v[70:73], v[118:121], v[156:159], v[86:89]
	s_waitcnt lgkmcnt(3)
	v_mfma_f32_16x16x32_f16 v[34:37], v[114:117], v[160:163], v[90:93]
	v_mfma_f32_16x16x32_f16 v[38:41], v[118:121], v[160:163], v[94:97]
	s_waitcnt lgkmcnt(2)
	v_mfma_f32_16x16x32_f16 v[74:77], v[114:117], v[148:151], v[98:101]
	v_mfma_f32_16x16x32_f16 v[78:81], v[118:121], v[148:151], v[102:105]
	s_waitcnt lgkmcnt(1)
	v_mfma_f32_16x16x32_f16 v[42:45], v[114:117], v[152:155], v[106:109]
	v_mfma_f32_16x16x32_f16 v[46:49], v[118:121], v[152:155], v[110:113]
	s_cbranch_vccz .LBB3_188
	s_and_b64 vcc, exec, s[6:7]
	s_cbranch_vccz .LBB3_189

.LBB3_139:
	s_barrier
	s_waitcnt lgkmcnt(0)
	ds_read_b128 v[82:85], v122 offset:20480
	ds_read_b128 v[86:89], v122 offset:22528
	ds_read_b128 v[90:93], v136
	s_and_b64 vcc, exec, s[4:5]
	s_waitcnt lgkmcnt(0)
	v_mfma_f32_16x16x32_f16 v[50:53], v[82:85], v[90:93], v[50:53]
	v_mfma_f32_16x16x32_f16 v[54:57], v[86:89], v[90:93], v[54:57]
	ds_read_b128 v[90:93], v136 offset:2048
	ds_read_b128 v[148:151], v136 offset:4096
	ds_read_b128 v[152:155], v136 offset:6144
	ds_read_b128 v[156:159], v136 offset:8192
	ds_read_b128 v[160:163], v136 offset:10240
	s_waitcnt lgkmcnt(4)
	v_mfma_f32_16x16x32_f16 v[18:21], v[82:85], v[90:93], v[18:21]
	v_mfma_f32_16x16x32_f16 v[22:25], v[86:89], v[90:93], v[22:25]
	s_waitcnt lgkmcnt(3)
	v_mfma_f32_16x16x32_f16 v[58:61], v[82:85], v[148:151], v[58:61]
	v_mfma_f32_16x16x32_f16 v[62:65], v[86:89], v[148:151], v[62:65]
	ds_read_b128 v[148:151], v136 offset:12288
	s_waitcnt lgkmcnt(3)
	v_mfma_f32_16x16x32_f16 v[26:29], v[82:85], v[152:155], v[26:29]
	v_mfma_f32_16x16x32_f16 v[30:33], v[86:89], v[152:155], v[30:33]
	ds_read_b128 v[152:155], v136 offset:14336
	s_waitcnt lgkmcnt(3)
	ds_read_b128 v[176:179], v136 offset:16384
	v_mfma_f32_16x16x32_f16 v[66:69], v[82:85], v[156:159], v[66:69]
	v_mfma_f32_16x16x32_f16 v[70:73], v[86:89], v[156:159], v[70:73]
	s_waitcnt lgkmcnt(3)
	v_mfma_f32_16x16x32_f16 v[34:37], v[82:85], v[160:163], v[34:37]
	v_mfma_f32_16x16x32_f16 v[38:41], v[86:89], v[160:163], v[38:41]
	s_waitcnt lgkmcnt(2)
	v_mfma_f32_16x16x32_f16 v[74:77], v[82:85], v[148:151], v[74:77]
	v_mfma_f32_16x16x32_f16 v[78:81], v[86:89], v[148:151], v[78:81]
	s_waitcnt lgkmcnt(1)
	v_mfma_f32_16x16x32_f16 v[42:45], v[82:85], v[152:155], v[42:45]
	v_mfma_f32_16x16x32_f16 v[46:49], v[86:89], v[152:155], v[46:49]
	s_cbranch_vccnz .LBB3_141
	s_waitcnt lgkmcnt(0)
	v_mfma_f32_16x16x32_f16 v[10:13], v[82:85], v[176:179], v[10:13]
	v_mfma_f32_16x16x32_f16 v[14:17], v[86:89], v[176:179], v[14:17]

.LBB3_143:
	s_waitcnt lgkmcnt(0)
	ds_read_b128 v[82:85], v123 offset:20480
	ds_read_b128 v[86:89], v123 offset:22528
	ds_read_b128 v[90:93], v137
	ds_read_b128 v[94:97], v137 offset:2048
	ds_read_b128 v[148:151], v137 offset:4096
	ds_read_b128 v[152:155], v137 offset:6144
	ds_read_b128 v[156:159], v137 offset:8192
	ds_read_b128 v[160:163], v137 offset:10240
	s_and_b64 vcc, exec, s[4:5]
	s_waitcnt lgkmcnt(5)
	v_mfma_f32_16x16x32_f16 v[50:53], v[82:85], v[90:93], v[50:53]
	v_mfma_f32_16x16x32_f16 v[54:57], v[86:89], v[90:93], v[54:57]
	s_waitcnt lgkmcnt(4)
	v_mfma_f32_16x16x32_f16 v[18:21], v[82:85], v[94:97], v[18:21]
	v_mfma_f32_16x16x32_f16 v[22:25], v[86:89], v[94:97], v[22:25]
	s_waitcnt lgkmcnt(3)
	v_mfma_f32_16x16x32_f16 v[58:61], v[82:85], v[148:151], v[58:61]
	v_mfma_f32_16x16x32_f16 v[62:65], v[86:89], v[148:151], v[62:65]
	ds_read_b128 v[148:151], v137 offset:12288
	s_waitcnt lgkmcnt(3)
	v_mfma_f32_16x16x32_f16 v[26:29], v[82:85], v[152:155], v[26:29]
	v_mfma_f32_16x16x32_f16 v[30:33], v[86:89], v[152:155], v[30:33]
	ds_read_b128 v[152:155], v137 offset:14336
	s_waitcnt lgkmcnt(3)
	ds_read_b128 v[176:179], v137 offset:16384
	v_mfma_f32_16x16x32_f16 v[66:69], v[82:85], v[156:159], v[66:69]
	v_mfma_f32_16x16x32_f16 v[70:73], v[86:89], v[156:159], v[70:73]
	s_waitcnt lgkmcnt(3)
	v_mfma_f32_16x16x32_f16 v[34:37], v[82:85], v[160:163], v[34:37]
	v_mfma_f32_16x16x32_f16 v[38:41], v[86:89], v[160:163], v[38:41]
	s_waitcnt lgkmcnt(2)
	v_mfma_f32_16x16x32_f16 v[74:77], v[82:85], v[148:151], v[74:77]
	v_mfma_f32_16x16x32_f16 v[78:81], v[86:89], v[148:151], v[78:81]
	s_waitcnt lgkmcnt(1)
	v_mfma_f32_16x16x32_f16 v[42:45], v[82:85], v[152:155], v[42:45]
	v_mfma_f32_16x16x32_f16 v[46:49], v[86:89], v[152:155], v[46:49]
	s_cbranch_vccnz .LBB3_145
	s_waitcnt lgkmcnt(0)
	v_mfma_f32_16x16x32_f16 v[10:13], v[82:85], v[176:179], v[10:13]
	v_mfma_f32_16x16x32_f16 v[14:17], v[86:89], v[176:179], v[14:17]

.LBB3_147:
	s_waitcnt vmcnt(0)
	s_barrier
	s_waitcnt lgkmcnt(0)
	ds_read_b128 v[118:121], v124 offset:53248
	ds_read_b128 v[122:125], v124 offset:55296
	ds_read_b128 v[82:85], v136 offset:53248
	s_and_b64 vcc, exec, s[4:5]
	s_waitcnt lgkmcnt(0)
	v_mfma_f32_16x16x32_f16 v[50:53], v[118:121], v[82:85], v[50:53]
	v_mfma_f32_16x16x32_f16 v[54:57], v[122:125], v[82:85], v[54:57]
	ds_read_b128 v[82:85], v136 offset:55296
	ds_read_b128 v[148:151], v136 offset:57344
	ds_read_b128 v[152:155], v136 offset:59392
	ds_read_b128 v[156:159], v136 offset:63488
	ds_read_b128 v[160:163], v136 offset:61440
	s_waitcnt lgkmcnt(4)
	v_mfma_f32_16x16x32_f16 v[98:101], v[122:125], v[82:85], v[22:25]
	s_nop 2
	v_mfma_f32_16x16x32_f16 v[94:97], v[118:121], v[82:85], v[18:21]
	s_waitcnt lgkmcnt(3)
	v_mfma_f32_16x16x32_f16 v[18:21], v[118:121], v[148:151], v[58:61]
	s_nop 2
	s_waitcnt lgkmcnt(2)
	v_mfma_f32_16x16x32_f16 v[102:105], v[118:121], v[152:155], v[26:29]
	v_mfma_f32_16x16x32_f16 v[106:109], v[122:125], v[152:155], v[30:33]
	ds_read_b128 v[152:155], v138 offset:12288
	s_nop 1
	s_waitcnt lgkmcnt(2)
	v_mfma_f32_16x16x32_f16 v[110:113], v[122:125], v[156:159], v[38:41]
	s_nop 2
	s_waitcnt lgkmcnt(0)
	ds_read_b128 v[176:179], v138 offset:16384
	v_mfma_f32_16x16x32_f16 v[82:85], v[118:121], v[152:155], v[74:77]
	v_mfma_f32_16x16x32_f16 v[86:89], v[122:125], v[152:155], v[78:81]
	ds_read_b128 v[152:155], v138 offset:14336
	v_mfma_f32_16x16x32_f16 v[22:25], v[122:125], v[148:151], v[62:65]
	v_mfma_f32_16x16x32_f16 v[26:29], v[118:121], v[160:163], v[66:69]
	v_mfma_f32_16x16x32_f16 v[30:33], v[122:125], v[160:163], v[70:73]
	v_mfma_f32_16x16x32_f16 v[34:37], v[118:121], v[156:159], v[34:37]
	s_waitcnt lgkmcnt(0)
	v_mfma_f32_16x16x32_f16 v[114:117], v[118:121], v[152:155], v[42:45]
	v_mfma_f32_16x16x32_f16 v[90:93], v[122:125], v[152:155], v[46:49]
	s_cbranch_vccnz .LBB3_149
	s_waitcnt lgkmcnt(0)
	v_mfma_f32_16x16x32_f16 v[10:13], v[118:121], v[176:179], v[10:13]
	v_mfma_f32_16x16x32_f16 v[14:17], v[122:125], v[176:179], v[14:17]

.LBB3_151:
	ds_read_b128 v[118:121], v140 offset:53248
	ds_read_b128 v[122:125], v140 offset:55296
	ds_read_b128 v[38:41], v137 offset:53248
	ds_read_b128 v[42:45], v137 offset:55296
	s_load_dwordx2 s[0:1], s[0:1], 0x10
	s_and_b64 vcc, exec, s[4:5]
	s_waitcnt lgkmcnt(0)
	v_mfma_f32_16x16x32_f16 v[78:81], v[118:121], v[38:41], v[50:53]
	v_mfma_f32_16x16x32_f16 v[74:77], v[122:125], v[38:41], v[54:57]
	v_mfma_f32_16x16x32_f16 v[70:73], v[118:121], v[42:45], v[94:97]
	v_mfma_f32_16x16x32_f16 v[66:69], v[122:125], v[42:45], v[98:101]
	ds_read_b128 v[38:41], v137 offset:57344
	ds_read_b128 v[42:45], v137 offset:59392
	s_waitcnt lgkmcnt(0)
	v_mfma_f32_16x16x32_f16 v[62:65], v[118:121], v[38:41], v[18:21]
	v_mfma_f32_16x16x32_f16 v[58:61], v[122:125], v[38:41], v[22:25]
	s_nop 1
	ds_read_b128 v[18:21], v137 offset:61440
	ds_read_b128 v[22:25], v137 offset:63488
	v_mfma_f32_16x16x32_f16 v[54:57], v[118:121], v[42:45], v[102:105]
	v_mfma_f32_16x16x32_f16 v[50:53], v[122:125], v[42:45], v[106:109]
	s_waitcnt lgkmcnt(0)
	ds_read_b128 v[176:179], v139 offset:16384
	v_mfma_f32_16x16x32_f16 v[46:49], v[118:121], v[18:21], v[26:29]
	v_mfma_f32_16x16x32_f16 v[42:45], v[122:125], v[18:21], v[30:33]
	v_mfma_f32_16x16x32_f16 v[38:41], v[118:121], v[22:25], v[34:37]
	v_mfma_f32_16x16x32_f16 v[34:37], v[122:125], v[22:25], v[110:113]
	ds_read_b128 v[18:21], v139 offset:12288
	ds_read_b128 v[22:25], v139 offset:14336
	s_waitcnt lgkmcnt(0)
	v_mfma_f32_16x16x32_f16 v[30:33], v[118:121], v[18:21], v[82:85]
	v_mfma_f32_16x16x32_f16 v[26:29], v[122:125], v[18:21], v[86:89]
	v_mfma_f32_16x16x32_f16 v[18:21], v[118:121], v[22:25], v[114:117]
	v_mfma_f32_16x16x32_f16 v[22:25], v[122:125], v[22:25], v[90:93]
	s_cbranch_vccnz .LBB3_153
	s_waitcnt lgkmcnt(0)
	v_mfma_f32_16x16x32_f16 v[10:13], v[118:121], v[176:179], v[10:13]
	v_mfma_f32_16x16x32_f16 v[14:17], v[122:125], v[176:179], v[14:17]

.LBB3_176:
	s_nop 1
	s_waitcnt lgkmcnt(0)
	v_mfma_f32_16x16x32_f16 v[10:13], v[86:89], v[176:179], v[10:13]
	v_mfma_f32_16x16x32_f16 v[14:17], v[90:93], v[176:179], v[14:17]
	v_cndmask_b32_e64 v82, 0, 1, s[12:13]
	v_cmp_ne_u32_e64 s[6:7], 1, v82
	s_andn2_b64 vcc, exec, s[12:13]
	s_cbranch_vccnz .LBB3_78

.LBB3_179:
	s_waitcnt lgkmcnt(0)
	v_mfma_f32_16x16x32_f16 v[10:13], v[86:89], v[176:179], v[10:13]
	v_mfma_f32_16x16x32_f16 v[14:17], v[90:93], v[176:179], v[14:17]
	s_and_b64 vcc, exec, s[6:7]
	s_cbranch_vccnz .LBB3_89

.LBB3_182:
	s_waitcnt lgkmcnt(0)
	v_mfma_f32_16x16x32_f16 v[10:13], v[82:85], v[176:179], v[10:13]
	v_mfma_f32_16x16x32_f16 v[14:17], v[86:89], v[176:179], v[14:17]
	s_and_b64 vcc, exec, s[6:7]
	s_cbranch_vccnz .LBB3_114

.LBB3_188:
	s_waitcnt lgkmcnt(0)
	v_mfma_f32_16x16x32_f16 v[10:13], v[114:117], v[176:179], v[10:13]
	v_mfma_f32_16x16x32_f16 v[14:17], v[118:121], v[176:179], v[14:17]
	s_and_b64 vcc, exec, s[6:7]
	s_cbranch_vccnz .LBB3_136

	.amdhsa_kernel _Z8moe_gemmILi1EEvPKDF16_S1_PvPKyPKiPKfS1_
		.amdhsa_group_segment_fixed_size 0
		.amdhsa_private_segment_fixed_size 0
		.amdhsa_kernarg_size 56
		.amdhsa_user_sgpr_count 2
		.amdhsa_user_sgpr_dispatch_ptr 0
		.amdhsa_user_sgpr_queue_ptr 0
		.amdhsa_user_sgpr_kernarg_segment_ptr 1
		.amdhsa_user_sgpr_dispatch_id 0
		.amdhsa_user_sgpr_kernarg_preload_length 0
		.amdhsa_user_sgpr_kernarg_preload_offset 0
		.amdhsa_user_sgpr_private_segment_size 0
		.amdhsa_uses_dynamic_stack 0
		.amdhsa_enable_private_segment 0
		.amdhsa_system_sgpr_workgroup_id_x 1
		.amdhsa_system_sgpr_workgroup_id_y 0
		.amdhsa_system_sgpr_workgroup_id_z 0
		.amdhsa_system_sgpr_workgroup_info 0
		.amdhsa_system_vgpr_workitem_id 0
		.amdhsa_next_free_vgpr 180
		.amdhsa_next_free_sgpr 94
		.amdhsa_accum_offset 180
		.amdhsa_reserve_vcc 1
		.amdhsa_float_round_mode_32 0
		.amdhsa_float_round_mode_16_64 0
		.amdhsa_float_denorm_mode_32 3
		.amdhsa_float_denorm_mode_16_64 3
		.amdhsa_dx10_clamp 1
		.amdhsa_ieee_mode 1
		.amdhsa_fp16_overflow 0
		.amdhsa_tg_split 0
		.amdhsa_exception_fp_ieee_invalid_op 0
		.amdhsa_exception_fp_denorm_src 0
		.amdhsa_exception_fp_ieee_div_zero 0
		.amdhsa_exception_fp_ieee_overflow 0
		.amdhsa_exception_fp_ieee_underflow 0
		.amdhsa_exception_fp_ieee_inexact 0
		.amdhsa_exception_int_div_zero 0
	.end_amdhsa_kernel

.LBB4_91:
	v_bitop3_b32 v0, v102, v0, 4 bitop3:0x36
	v_lshlrev_b32_e32 v143, 4, v0
	v_add_u32_e32 v0, v34, v143
	v_add_u32_e32 v139, 0, v0
	ds_read_b128 v[102:105], v139 offset:20480
	v_or_b32_e32 v147, v143, v140
	v_add_u32_e32 v0, 0, v147
	ds_read_b128 v[106:109], v139 offset:22528
	ds_read_b128 v[26:29], v0
	ds_read_b128 v[50:53], v0 offset:2048
	s_waitcnt lgkmcnt(0)
	v_mfma_f32_16x16x32_f16 v[38:41], v[106:109], v[26:29], v[46:49]
	s_andn2_b64 vcc, exec, s[26:27]
	v_mfma_f32_16x16x32_f16 v[34:37], v[102:105], v[26:29], v[42:45]
	ds_read_b128 v[26:29], v0 offset:4096
	ds_read_b128 v[62:65], v0 offset:6144
	v_mfma_f32_16x16x32_f16 v[42:45], v[102:105], v[50:53], v[54:57]
	v_mfma_f32_16x16x32_f16 v[46:49], v[106:109], v[50:53], v[58:61]
	s_waitcnt lgkmcnt(0)
	v_mfma_f32_16x16x32_f16 v[50:53], v[102:105], v[26:29], v[66:69]
	v_mfma_f32_16x16x32_f16 v[54:57], v[106:109], v[26:29], v[70:73]
	v_mfma_f32_16x16x32_f16 v[58:61], v[102:105], v[62:65], v[74:77]
	v_mfma_f32_16x16x32_f16 v[62:65], v[106:109], v[62:65], v[78:81]
	ds_read_b128 v[26:29], v0 offset:8192
	s_nop 1
	ds_read_b128 v[78:81], v0 offset:10240
	s_waitcnt lgkmcnt(0)
	ds_read_b128 v[184:187], v0 offset:16384
	v_mfma_f32_16x16x32_f16 v[66:69], v[102:105], v[26:29], v[82:85]
	s_nop 2
	v_cndmask_b32_e64 v82, 0, 1, s[26:27]
	v_mfma_f32_16x16x32_f16 v[70:73], v[106:109], v[26:29], v[22:25]
	v_cmp_ne_u32_e64 s[24:25], 1, v82
	v_mfma_f32_16x16x32_f16 v[74:77], v[102:105], v[78:81], v[86:89]
	v_mfma_f32_16x16x32_f16 v[18:21], v[106:109], v[78:81], v[18:21]
	ds_read_b128 v[26:29], v0 offset:12288
	ds_read_b128 v[78:81], v0 offset:14336
	s_waitcnt lgkmcnt(0)
	v_mfma_f32_16x16x32_f16 v[22:25], v[102:105], v[26:29], v[90:93]
	v_mfma_f32_16x16x32_f16 v[26:29], v[106:109], v[26:29], v[30:33]
	v_mfma_f32_16x16x32_f16 v[30:33], v[102:105], v[78:81], v[94:97]
	v_mfma_f32_16x16x32_f16 v[78:81], v[106:109], v[78:81], v[98:101]
	s_cbranch_vccz .LBB4_186
	v_cndmask_b32_e64 v82, 0, 1, s[28:29]
	v_cmp_ne_u32_e64 s[26:27], 1, v82
	s_andn2_b64 vcc, exec, s[28:29]
	s_cbranch_vccz .LBB4_187

.LBB4_98:
	v_add_u32_e32 v82, s36, v140
	v_add_u32_e32 v107, 0x5000, v82
	v_or_b32_e32 v106, v107, v141
	v_add_u32_e32 v142, 0, v106
	ds_read_b128 v[98:101], v142 offset:53248
	ds_read_b128 v[102:105], v142 offset:55296
	ds_read_b128 v[82:85], v137 offset:53248
	ds_read_b128 v[86:89], v137 offset:55296
	v_add_u32_e32 v140, 0xd000, v137
	s_and_b64 vcc, exec, s[24:25]
	s_waitcnt lgkmcnt(0)
	v_mfma_f32_16x16x32_f16 v[34:37], v[98:101], v[82:85], v[34:37]
	s_mov_b32 m0, s76
	v_mfma_f32_16x16x32_f16 v[38:41], v[102:105], v[82:85], v[38:41]
	global_load_lds_dwordx4 v176, s[72:73]
	v_mfma_f32_16x16x32_f16 v[42:45], v[98:101], v[86:89], v[42:45]
	s_mov_b32 m0, s77
	v_mfma_f32_16x16x32_f16 v[46:49], v[102:105], v[86:89], v[46:49]
	global_load_lds_dwordx4 v177, s[72:73]
	ds_read_b128 v[82:85], v137 offset:57344
	ds_read_b128 v[86:89], v137 offset:59392
	s_waitcnt lgkmcnt(0)
	v_mfma_f32_16x16x32_f16 v[50:53], v[98:101], v[82:85], v[50:53]
	s_mov_b32 m0, s78
	v_mfma_f32_16x16x32_f16 v[54:57], v[102:105], v[82:85], v[54:57]
	global_load_lds_dwordx4 v178, s[72:73]
	v_mfma_f32_16x16x32_f16 v[58:61], v[98:101], v[86:89], v[58:61]
	s_mov_b32 m0, s79
	v_mfma_f32_16x16x32_f16 v[62:65], v[102:105], v[86:89], v[62:65]
	global_load_lds_dwordx4 v179, s[72:73]
	ds_read_b128 v[82:85], v137 offset:61440
	ds_read_b128 v[86:89], v137 offset:63488
	s_waitcnt lgkmcnt(0)
	ds_read_b128 v[184:187], v140 offset:16384
	v_mfma_f32_16x16x32_f16 v[66:69], v[98:101], v[82:85], v[66:69]
	s_mov_b32 m0, s80
	v_mfma_f32_16x16x32_f16 v[70:73], v[102:105], v[82:85], v[70:73]
	global_load_lds_dwordx4 v180, s[74:75]
	v_mfma_f32_16x16x32_f16 v[82:85], v[102:105], v[86:89], v[18:21]
	s_nop 2
	ds_read_b128 v[18:21], v140 offset:12288
	ds_read_b128 v[148:151], v140 offset:14336
	s_mov_b32 m0, s81
	v_mfma_f32_16x16x32_f16 v[74:77], v[98:101], v[86:89], v[74:77]
	global_load_lds_dwordx4 v181, s[74:75]
	s_waitcnt lgkmcnt(0)
	v_mfma_f32_16x16x32_f16 v[86:89], v[98:101], v[18:21], v[22:25]
	v_mfma_f32_16x16x32_f16 v[90:93], v[102:105], v[18:21], v[26:29]
	v_mfma_f32_16x16x32_f16 v[94:97], v[98:101], v[148:151], v[30:33]
	v_mfma_f32_16x16x32_f16 v[78:81], v[102:105], v[148:151], v[78:81]
	s_cbranch_vccnz .LBB4_100
	s_waitcnt lgkmcnt(0)
	v_mfma_f32_16x16x32_f16 v[6:9], v[98:101], v[184:187], v[6:9]
	v_mfma_f32_16x16x32_f16 v[2:5], v[102:105], v[184:187], v[2:5]

.LBB4_102:
	v_or_b32_e32 v107, v107, v143
	v_add_u32_e32 v143, 0, v107
	ds_read_b128 v[98:101], v143 offset:53248
	ds_read_b128 v[102:105], v143 offset:55296
	ds_read_b128 v[22:25], v0 offset:53248
	ds_read_b128 v[30:33], v0 offset:55296
	v_add_u32_e32 v141, 0xd000, v0
	s_and_b64 vcc, exec, s[24:25]
	s_waitcnt lgkmcnt(0)
	v_mfma_f32_16x16x32_f16 v[18:21], v[98:101], v[22:25], v[34:37]
	v_mfma_f32_16x16x32_f16 v[22:25], v[102:105], v[22:25], v[38:41]
	v_mfma_f32_16x16x32_f16 v[26:29], v[98:101], v[30:33], v[42:45]
	v_mfma_f32_16x16x32_f16 v[30:33], v[102:105], v[30:33], v[46:49]
	s_nop 0
	ds_read_b128 v[38:41], v0 offset:57344
	s_nop 0
	ds_read_b128 v[46:49], v0 offset:59392
	s_waitcnt lgkmcnt(0)
	v_mfma_f32_16x16x32_f16 v[34:37], v[98:101], v[38:41], v[50:53]
	v_mfma_f32_16x16x32_f16 v[38:41], v[102:105], v[38:41], v[54:57]
	v_mfma_f32_16x16x32_f16 v[42:45], v[98:101], v[46:49], v[58:61]
	v_mfma_f32_16x16x32_f16 v[46:49], v[102:105], v[46:49], v[62:65]
	s_nop 0
	ds_read_b128 v[54:57], v0 offset:61440
	s_nop 0
	ds_read_b128 v[62:65], v0 offset:63488
	s_waitcnt lgkmcnt(0)
	ds_read_b128 v[184:187], v141 offset:16384
	v_mfma_f32_16x16x32_f16 v[50:53], v[98:101], v[54:57], v[66:69]
	v_mfma_f32_16x16x32_f16 v[54:57], v[102:105], v[54:57], v[70:73]
	v_mfma_f32_16x16x32_f16 v[58:61], v[98:101], v[62:65], v[74:77]
	v_mfma_f32_16x16x32_f16 v[62:65], v[102:105], v[62:65], v[82:85]
	s_nop 0
	ds_read_b128 v[70:73], v141 offset:12288
	s_nop 0
	ds_read_b128 v[82:85], v141 offset:14336
	s_waitcnt lgkmcnt(0)
	v_mfma_f32_16x16x32_f16 v[66:69], v[98:101], v[70:73], v[86:89]
	v_mfma_f32_16x16x32_f16 v[70:73], v[102:105], v[70:73], v[90:93]
	v_mfma_f32_16x16x32_f16 v[74:77], v[98:101], v[82:85], v[94:97]
	v_mfma_f32_16x16x32_f16 v[78:81], v[102:105], v[82:85], v[78:81]
	s_cbranch_vccz .LBB4_189
	s_and_b64 vcc, exec, s[26:27]
	s_cbranch_vccz .LBB4_190

.LBB4_109:
	s_and_b64 vcc, exec, s[24:25]
	s_waitcnt lgkmcnt(5)
	v_mfma_f32_16x16x32_f16 v[22:25], v[86:89], v[92:95], v[22:25]
	s_mov_b32 m0, s82
	v_mfma_f32_16x16x32_f16 v[18:21], v[82:85], v[92:95], v[18:21]
	global_load_lds_dwordx4 v176, s[72:73]
	s_waitcnt lgkmcnt(4)
	v_mfma_f32_16x16x32_f16 v[26:29], v[82:85], v[96:99], v[26:29]
	s_mov_b32 m0, s83
	v_mfma_f32_16x16x32_f16 v[30:33], v[86:89], v[96:99], v[30:33]
	global_load_lds_dwordx4 v177, s[72:73]
	s_waitcnt lgkmcnt(3)
	v_mfma_f32_16x16x32_f16 v[34:37], v[82:85], v[156:159], v[34:37]
	s_mov_b32 m0, s84
	v_mfma_f32_16x16x32_f16 v[38:41], v[86:89], v[156:159], v[38:41]
	global_load_lds_dwordx4 v178, s[72:73]
	ds_read_b128 v[156:159], v146 offset:12288
	s_waitcnt lgkmcnt(3)
	v_mfma_f32_16x16x32_f16 v[42:45], v[82:85], v[160:163], v[42:45]
	s_mov_b32 m0, s85
	v_mfma_f32_16x16x32_f16 v[46:49], v[86:89], v[160:163], v[46:49]
	global_load_lds_dwordx4 v179, s[72:73]
	ds_read_b128 v[160:163], v146 offset:14336
	s_waitcnt lgkmcnt(3)
	ds_read_b128 v[184:187], v146 offset:16384
	v_mfma_f32_16x16x32_f16 v[50:53], v[82:85], v[164:167], v[50:53]
	s_mov_b32 m0, s86
	v_mfma_f32_16x16x32_f16 v[54:57], v[86:89], v[164:167], v[54:57]
	global_load_lds_dwordx4 v180, s[74:75]
	s_waitcnt lgkmcnt(3)
	v_mfma_f32_16x16x32_f16 v[58:61], v[82:85], v[168:171], v[58:61]
	s_mov_b32 m0, s87
	v_mfma_f32_16x16x32_f16 v[62:65], v[86:89], v[168:171], v[62:65]
	global_load_lds_dwordx4 v181, s[74:75]
	s_waitcnt lgkmcnt(2)
	v_mfma_f32_16x16x32_f16 v[66:69], v[82:85], v[156:159], v[66:69]
	v_mfma_f32_16x16x32_f16 v[70:73], v[86:89], v[156:159], v[70:73]
	s_waitcnt lgkmcnt(1)
	v_mfma_f32_16x16x32_f16 v[74:77], v[82:85], v[160:163], v[74:77]
	v_mfma_f32_16x16x32_f16 v[78:81], v[86:89], v[160:163], v[78:81]
	s_cbranch_vccnz .LBB4_111
	s_waitcnt lgkmcnt(0)
	v_mfma_f32_16x16x32_f16 v[6:9], v[82:85], v[184:187], v[6:9]
	v_mfma_f32_16x16x32_f16 v[2:5], v[86:89], v[184:187], v[2:5]

.LBB4_113:
	s_waitcnt lgkmcnt(0)
	v_add_u32_e32 v148, s35, v107
	ds_read_b128 v[82:85], v148
	ds_read_b128 v[86:89], v148 offset:2048
	v_add_u32_e32 v147, s35, v147
	ds_read_b128 v[92:95], v147
	ds_read_b128 v[96:99], v147 offset:2048
	ds_read_b128 v[156:159], v147 offset:4096
	ds_read_b128 v[160:163], v147 offset:6144
	ds_read_b128 v[164:167], v147 offset:8192
	ds_read_b128 v[168:171], v147 offset:10240
	s_and_b64 vcc, exec, s[24:25]
	s_waitcnt lgkmcnt(5)
	v_mfma_f32_16x16x32_f16 v[22:25], v[86:89], v[92:95], v[22:25]
	v_mfma_f32_16x16x32_f16 v[18:21], v[82:85], v[92:95], v[18:21]
	s_waitcnt lgkmcnt(4)
	v_mfma_f32_16x16x32_f16 v[26:29], v[82:85], v[96:99], v[26:29]
	v_mfma_f32_16x16x32_f16 v[30:33], v[86:89], v[96:99], v[30:33]
	s_waitcnt lgkmcnt(3)
	v_mfma_f32_16x16x32_f16 v[34:37], v[82:85], v[156:159], v[34:37]
	v_mfma_f32_16x16x32_f16 v[38:41], v[86:89], v[156:159], v[38:41]
	ds_read_b128 v[156:159], v147 offset:12288
	s_waitcnt lgkmcnt(3)
	v_mfma_f32_16x16x32_f16 v[42:45], v[82:85], v[160:163], v[42:45]
	v_mfma_f32_16x16x32_f16 v[46:49], v[86:89], v[160:163], v[46:49]
	ds_read_b128 v[160:163], v147 offset:14336
	s_waitcnt lgkmcnt(3)
	ds_read_b128 v[184:187], v147 offset:16384
	v_mfma_f32_16x16x32_f16 v[50:53], v[82:85], v[164:167], v[50:53]
	v_mfma_f32_16x16x32_f16 v[54:57], v[86:89], v[164:167], v[54:57]
	s_waitcnt lgkmcnt(3)
	v_mfma_f32_16x16x32_f16 v[58:61], v[82:85], v[168:171], v[58:61]
	v_mfma_f32_16x16x32_f16 v[62:65], v[86:89], v[168:171], v[62:65]
	s_waitcnt lgkmcnt(2)
	v_mfma_f32_16x16x32_f16 v[66:69], v[82:85], v[156:159], v[66:69]
	v_mfma_f32_16x16x32_f16 v[70:73], v[86:89], v[156:159], v[70:73]
	s_waitcnt lgkmcnt(1)
	v_mfma_f32_16x16x32_f16 v[74:77], v[82:85], v[160:163], v[74:77]
	v_mfma_f32_16x16x32_f16 v[78:81], v[86:89], v[160:163], v[78:81]
	s_cbranch_vccnz .LBB4_115
	s_waitcnt lgkmcnt(0)
	v_mfma_f32_16x16x32_f16 v[6:9], v[82:85], v[184:187], v[6:9]
	v_mfma_f32_16x16x32_f16 v[2:5], v[86:89], v[184:187], v[2:5]

.LBB4_123:
	s_and_b64 vcc, exec, s[24:25]
	s_waitcnt lgkmcnt(5)
	v_mfma_f32_16x16x32_f16 v[18:21], v[82:85], v[92:95], v[18:21]
	s_mov_b32 m0, s88
	v_mfma_f32_16x16x32_f16 v[22:25], v[86:89], v[92:95], v[22:25]
	global_load_lds_dwordx4 v176, s[72:73]
	s_waitcnt lgkmcnt(4)
	v_mfma_f32_16x16x32_f16 v[26:29], v[82:85], v[96:99], v[26:29]
	s_mov_b32 m0, s89
	v_mfma_f32_16x16x32_f16 v[30:33], v[86:89], v[96:99], v[30:33]
	global_load_lds_dwordx4 v177, s[72:73]
	s_waitcnt lgkmcnt(3)
	v_mfma_f32_16x16x32_f16 v[34:37], v[82:85], v[156:159], v[34:37]
	s_mov_b32 m0, s90
	v_mfma_f32_16x16x32_f16 v[38:41], v[86:89], v[156:159], v[38:41]
	global_load_lds_dwordx4 v178, s[72:73]
	ds_read_b128 v[156:159], v137 offset:12288
	s_waitcnt lgkmcnt(3)
	v_mfma_f32_16x16x32_f16 v[42:45], v[82:85], v[160:163], v[42:45]
	s_mov_b32 m0, s91
	v_mfma_f32_16x16x32_f16 v[46:49], v[86:89], v[160:163], v[46:49]
	global_load_lds_dwordx4 v179, s[72:73]
	ds_read_b128 v[160:163], v137 offset:14336
	s_waitcnt lgkmcnt(3)
	ds_read_b128 v[184:187], v137 offset:16384
	v_mfma_f32_16x16x32_f16 v[50:53], v[82:85], v[164:167], v[50:53]
	s_mov_b32 m0, s92
	v_mfma_f32_16x16x32_f16 v[54:57], v[86:89], v[164:167], v[54:57]
	global_load_lds_dwordx4 v180, s[74:75]
	s_waitcnt lgkmcnt(3)
	v_mfma_f32_16x16x32_f16 v[58:61], v[82:85], v[168:171], v[58:61]
	s_mov_b32 m0, s93
	v_mfma_f32_16x16x32_f16 v[62:65], v[86:89], v[168:171], v[62:65]
	global_load_lds_dwordx4 v181, s[74:75]
	s_waitcnt lgkmcnt(2)
	v_mfma_f32_16x16x32_f16 v[66:69], v[82:85], v[156:159], v[66:69]
	v_mfma_f32_16x16x32_f16 v[70:73], v[86:89], v[156:159], v[70:73]
	s_waitcnt lgkmcnt(1)
	v_mfma_f32_16x16x32_f16 v[74:77], v[82:85], v[160:163], v[74:77]
	v_mfma_f32_16x16x32_f16 v[78:81], v[86:89], v[160:163], v[78:81]
	s_cbranch_vccnz .LBB4_125
	s_waitcnt lgkmcnt(0)
	v_mfma_f32_16x16x32_f16 v[6:9], v[82:85], v[184:187], v[6:9]
	v_mfma_f32_16x16x32_f16 v[2:5], v[86:89], v[184:187], v[2:5]

.LBB4_127:
	s_waitcnt lgkmcnt(0)
	ds_read_b128 v[82:85], v139 offset:20480
	ds_read_b128 v[86:89], v139 offset:22528
	ds_read_b128 v[92:95], v0
	ds_read_b128 v[96:99], v0 offset:2048
	ds_read_b128 v[156:159], v0 offset:4096
	ds_read_b128 v[160:163], v0 offset:6144
	ds_read_b128 v[164:167], v0 offset:8192
	ds_read_b128 v[168:171], v0 offset:10240
	s_and_b64 vcc, exec, s[24:25]
	s_waitcnt lgkmcnt(5)
	v_mfma_f32_16x16x32_f16 v[18:21], v[82:85], v[92:95], v[18:21]
	v_mfma_f32_16x16x32_f16 v[22:25], v[86:89], v[92:95], v[22:25]
	s_waitcnt lgkmcnt(4)
	v_mfma_f32_16x16x32_f16 v[26:29], v[82:85], v[96:99], v[26:29]
	v_mfma_f32_16x16x32_f16 v[30:33], v[86:89], v[96:99], v[30:33]
	s_waitcnt lgkmcnt(3)
	v_mfma_f32_16x16x32_f16 v[34:37], v[82:85], v[156:159], v[34:37]
	v_mfma_f32_16x16x32_f16 v[38:41], v[86:89], v[156:159], v[38:41]
	ds_read_b128 v[156:159], v0 offset:12288
	s_waitcnt lgkmcnt(3)
	v_mfma_f32_16x16x32_f16 v[42:45], v[82:85], v[160:163], v[42:45]
	v_mfma_f32_16x16x32_f16 v[46:49], v[86:89], v[160:163], v[46:49]
	ds_read_b128 v[160:163], v0 offset:14336
	s_waitcnt lgkmcnt(3)
	ds_read_b128 v[184:187], v0 offset:16384
	v_mfma_f32_16x16x32_f16 v[50:53], v[82:85], v[164:167], v[50:53]
	v_mfma_f32_16x16x32_f16 v[54:57], v[86:89], v[164:167], v[54:57]
	s_waitcnt lgkmcnt(3)
	v_mfma_f32_16x16x32_f16 v[58:61], v[82:85], v[168:171], v[58:61]
	v_mfma_f32_16x16x32_f16 v[62:65], v[86:89], v[168:171], v[62:65]
	s_waitcnt lgkmcnt(2)
	v_mfma_f32_16x16x32_f16 v[66:69], v[82:85], v[156:159], v[66:69]
	v_mfma_f32_16x16x32_f16 v[70:73], v[86:89], v[156:159], v[70:73]
	s_waitcnt lgkmcnt(1)
	v_mfma_f32_16x16x32_f16 v[74:77], v[82:85], v[160:163], v[74:77]
	v_mfma_f32_16x16x32_f16 v[78:81], v[86:89], v[160:163], v[78:81]
	s_cbranch_vccz .LBB4_192
	s_and_b64 vcc, exec, s[26:27]
	s_cbranch_vccz .LBB4_193

.LBB4_134:
	s_and_b64 vcc, exec, s[24:25]
	s_waitcnt lgkmcnt(5)
	v_mfma_f32_16x16x32_f16 v[18:21], v[82:85], v[92:95], v[18:21]
	s_mov_b32 m0, s76
	v_mfma_f32_16x16x32_f16 v[22:25], v[86:89], v[92:95], v[22:25]
	global_load_lds_dwordx4 v176, s[72:73]
	s_waitcnt lgkmcnt(4)
	v_mfma_f32_16x16x32_f16 v[26:29], v[82:85], v[96:99], v[26:29]
	s_mov_b32 m0, s77
	v_mfma_f32_16x16x32_f16 v[30:33], v[86:89], v[96:99], v[30:33]
	global_load_lds_dwordx4 v177, s[72:73]
	s_waitcnt lgkmcnt(3)
	v_mfma_f32_16x16x32_f16 v[34:37], v[82:85], v[156:159], v[34:37]
	s_mov_b32 m0, s78
	v_mfma_f32_16x16x32_f16 v[38:41], v[86:89], v[156:159], v[38:41]
	global_load_lds_dwordx4 v178, s[72:73]
	ds_read_b128 v[156:159], v140 offset:12288
	s_waitcnt lgkmcnt(3)
	v_mfma_f32_16x16x32_f16 v[42:45], v[82:85], v[160:163], v[42:45]
	s_mov_b32 m0, s79
	v_mfma_f32_16x16x32_f16 v[46:49], v[86:89], v[160:163], v[46:49]
	global_load_lds_dwordx4 v179, s[72:73]
	ds_read_b128 v[160:163], v140 offset:14336
	s_waitcnt lgkmcnt(3)
	ds_read_b128 v[184:187], v140 offset:16384
	v_mfma_f32_16x16x32_f16 v[50:53], v[82:85], v[164:167], v[50:53]
	s_mov_b32 m0, s80
	v_mfma_f32_16x16x32_f16 v[54:57], v[86:89], v[164:167], v[54:57]
	global_load_lds_dwordx4 v180, s[74:75]
	s_waitcnt lgkmcnt(3)
	v_mfma_f32_16x16x32_f16 v[58:61], v[82:85], v[168:171], v[58:61]
	s_mov_b32 m0, s81
	v_mfma_f32_16x16x32_f16 v[62:65], v[86:89], v[168:171], v[62:65]
	global_load_lds_dwordx4 v181, s[74:75]
	s_waitcnt lgkmcnt(2)
	v_mfma_f32_16x16x32_f16 v[66:69], v[82:85], v[156:159], v[66:69]
	v_mfma_f32_16x16x32_f16 v[70:73], v[86:89], v[156:159], v[70:73]
	s_waitcnt lgkmcnt(1)
	v_mfma_f32_16x16x32_f16 v[74:77], v[82:85], v[160:163], v[74:77]
	v_mfma_f32_16x16x32_f16 v[78:81], v[86:89], v[160:163], v[78:81]
	s_cbranch_vccnz .LBB4_136
	s_waitcnt lgkmcnt(0)
	v_mfma_f32_16x16x32_f16 v[6:9], v[82:85], v[184:187], v[6:9]
	v_mfma_f32_16x16x32_f16 v[2:5], v[86:89], v[184:187], v[2:5]

.LBB4_138:
	s_waitcnt lgkmcnt(0)
	ds_read_b128 v[82:85], v143 offset:53248
	ds_read_b128 v[86:89], v143 offset:55296
	ds_read_b128 v[92:95], v0 offset:53248
	ds_read_b128 v[96:99], v0 offset:55296
	ds_read_b128 v[156:159], v0 offset:57344
	ds_read_b128 v[160:163], v0 offset:59392
	ds_read_b128 v[164:167], v0 offset:61440
	ds_read_b128 v[168:171], v0 offset:63488
	s_and_b64 vcc, exec, s[24:25]
	s_waitcnt lgkmcnt(5)
	v_mfma_f32_16x16x32_f16 v[18:21], v[82:85], v[92:95], v[18:21]
	v_mfma_f32_16x16x32_f16 v[22:25], v[86:89], v[92:95], v[22:25]
	s_waitcnt lgkmcnt(4)
	v_mfma_f32_16x16x32_f16 v[26:29], v[82:85], v[96:99], v[26:29]
	v_mfma_f32_16x16x32_f16 v[30:33], v[86:89], v[96:99], v[30:33]
	s_waitcnt lgkmcnt(3)
	v_mfma_f32_16x16x32_f16 v[34:37], v[82:85], v[156:159], v[34:37]
	v_mfma_f32_16x16x32_f16 v[38:41], v[86:89], v[156:159], v[38:41]
	ds_read_b128 v[156:159], v141 offset:12288
	s_waitcnt lgkmcnt(3)
	v_mfma_f32_16x16x32_f16 v[42:45], v[82:85], v[160:163], v[42:45]
	v_mfma_f32_16x16x32_f16 v[46:49], v[86:89], v[160:163], v[46:49]
	ds_read_b128 v[160:163], v141 offset:14336
	s_waitcnt lgkmcnt(3)
	ds_read_b128 v[184:187], v141 offset:16384
	v_mfma_f32_16x16x32_f16 v[50:53], v[82:85], v[164:167], v[50:53]
	v_mfma_f32_16x16x32_f16 v[54:57], v[86:89], v[164:167], v[54:57]
	s_waitcnt lgkmcnt(3)
	v_mfma_f32_16x16x32_f16 v[58:61], v[82:85], v[168:171], v[58:61]
	v_mfma_f32_16x16x32_f16 v[62:65], v[86:89], v[168:171], v[62:65]
	s_waitcnt lgkmcnt(2)
	v_mfma_f32_16x16x32_f16 v[66:69], v[82:85], v[156:159], v[66:69]
	v_mfma_f32_16x16x32_f16 v[70:73], v[86:89], v[156:159], v[70:73]
	s_waitcnt lgkmcnt(1)
	v_mfma_f32_16x16x32_f16 v[74:77], v[82:85], v[160:163], v[74:77]
	v_mfma_f32_16x16x32_f16 v[78:81], v[86:89], v[160:163], v[78:81]
	s_cbranch_vccz .LBB4_195
	s_and_b64 vcc, exec, s[26:27]
	s_cbranch_vccz .LBB4_196

.LBB4_145:
	s_waitcnt lgkmcnt(0)
	ds_read_b128 v[114:117], v90
	ds_read_b128 v[118:121], v90 offset:2048
	ds_read_b128 v[82:85], v146
	ds_read_b128 v[86:89], v146 offset:2048
	ds_read_b128 v[156:159], v146 offset:4096
	ds_read_b128 v[160:163], v146 offset:6144
	ds_read_b128 v[164:167], v146 offset:8192
	ds_read_b128 v[168:171], v146 offset:10240
	s_and_b64 vcc, exec, s[24:25]
	s_waitcnt lgkmcnt(5)
	v_mfma_f32_16x16x32_f16 v[18:21], v[114:117], v[82:85], v[18:21]
	s_mov_b32 m0, s82
	v_mfma_f32_16x16x32_f16 v[22:25], v[118:121], v[82:85], v[22:25]
	global_load_lds_dwordx4 v176, s[72:73]
	s_waitcnt lgkmcnt(4)
	v_mfma_f32_16x16x32_f16 v[26:29], v[114:117], v[86:89], v[26:29]
	s_mov_b32 m0, s83
	v_mfma_f32_16x16x32_f16 v[30:33], v[118:121], v[86:89], v[30:33]
	global_load_lds_dwordx4 v177, s[72:73]
	s_waitcnt lgkmcnt(2)
	v_mfma_f32_16x16x32_f16 v[42:45], v[114:117], v[160:163], v[42:45]
	s_mov_b32 m0, s84
	v_mfma_f32_16x16x32_f16 v[46:49], v[118:121], v[160:163], v[46:49]
	global_load_lds_dwordx4 v178, s[72:73]
	v_mfma_f32_16x16x32_f16 v[34:37], v[114:117], v[156:159], v[34:37]
	s_mov_b32 m0, s85
	v_mfma_f32_16x16x32_f16 v[38:41], v[118:121], v[156:159], v[38:41]
	global_load_lds_dwordx4 v179, s[72:73]
	ds_read_b128 v[156:159], v146 offset:12288
	ds_read_b128 v[160:163], v146 offset:14336
	s_waitcnt lgkmcnt(3)
	ds_read_b128 v[184:187], v146 offset:16384
	v_mfma_f32_16x16x32_f16 v[82:85], v[114:117], v[164:167], v[50:53]
	s_mov_b32 m0, s86
	v_mfma_f32_16x16x32_f16 v[86:89], v[118:121], v[164:167], v[54:57]
	global_load_lds_dwordx4 v180, s[74:75]
	s_nop 1
	s_waitcnt lgkmcnt(3)
	v_mfma_f32_16x16x32_f16 v[90:93], v[114:117], v[168:171], v[58:61]
	s_mov_b32 m0, s87
	v_mfma_f32_16x16x32_f16 v[94:97], v[118:121], v[168:171], v[62:65]
	global_load_lds_dwordx4 v181, s[74:75]
	s_waitcnt lgkmcnt(2)
	v_mfma_f32_16x16x32_f16 v[98:101], v[114:117], v[156:159], v[66:69]
	v_mfma_f32_16x16x32_f16 v[102:105], v[118:121], v[156:159], v[70:73]
	s_waitcnt lgkmcnt(1)
	v_mfma_f32_16x16x32_f16 v[106:109], v[114:117], v[160:163], v[74:77]
	v_mfma_f32_16x16x32_f16 v[110:113], v[118:121], v[160:163], v[78:81]
	s_cbranch_vccnz .LBB4_147
	s_waitcnt lgkmcnt(0)
	v_mfma_f32_16x16x32_f16 v[6:9], v[114:117], v[184:187], v[6:9]
	v_mfma_f32_16x16x32_f16 v[2:5], v[118:121], v[184:187], v[2:5]

.LBB4_149:
	s_waitcnt lgkmcnt(0)
	ds_read_b128 v[114:117], v148
	ds_read_b128 v[118:121], v148 offset:2048
	ds_read_b128 v[54:57], v147
	ds_read_b128 v[58:61], v147 offset:2048
	ds_read_b128 v[156:159], v147 offset:4096
	ds_read_b128 v[160:163], v147 offset:6144
	ds_read_b128 v[164:167], v147 offset:8192
	ds_read_b128 v[168:171], v147 offset:10240
	s_and_b64 vcc, exec, s[24:25]
	s_waitcnt lgkmcnt(5)
	v_mfma_f32_16x16x32_f16 v[50:53], v[114:117], v[54:57], v[18:21]
	v_mfma_f32_16x16x32_f16 v[54:57], v[118:121], v[54:57], v[22:25]
	s_waitcnt lgkmcnt(4)
	v_mfma_f32_16x16x32_f16 v[18:21], v[114:117], v[58:61], v[26:29]
	v_mfma_f32_16x16x32_f16 v[22:25], v[118:121], v[58:61], v[30:33]
	s_nop 1
	s_waitcnt lgkmcnt(3)
	v_mfma_f32_16x16x32_f16 v[58:61], v[114:117], v[156:159], v[34:37]
	v_mfma_f32_16x16x32_f16 v[62:65], v[118:121], v[156:159], v[38:41]
	ds_read_b128 v[156:159], v147 offset:12288
	s_nop 1
	s_waitcnt lgkmcnt(3)
	v_mfma_f32_16x16x32_f16 v[26:29], v[114:117], v[160:163], v[42:45]
	v_mfma_f32_16x16x32_f16 v[30:33], v[118:121], v[160:163], v[46:49]
	ds_read_b128 v[160:163], v147 offset:14336
	s_nop 1
	s_waitcnt lgkmcnt(3)
	ds_read_b128 v[184:187], v147 offset:16384
	v_mfma_f32_16x16x32_f16 v[66:69], v[114:117], v[164:167], v[82:85]
	v_mfma_f32_16x16x32_f16 v[70:73], v[118:121], v[164:167], v[86:89]
	s_waitcnt lgkmcnt(3)
	v_mfma_f32_16x16x32_f16 v[34:37], v[114:117], v[168:171], v[90:93]
	v_mfma_f32_16x16x32_f16 v[38:41], v[118:121], v[168:171], v[94:97]
	s_waitcnt lgkmcnt(2)
	v_mfma_f32_16x16x32_f16 v[74:77], v[114:117], v[156:159], v[98:101]
	v_mfma_f32_16x16x32_f16 v[78:81], v[118:121], v[156:159], v[102:105]
	s_waitcnt lgkmcnt(1)
	v_mfma_f32_16x16x32_f16 v[42:45], v[114:117], v[160:163], v[106:109]
	v_mfma_f32_16x16x32_f16 v[46:49], v[118:121], v[160:163], v[110:113]
	s_cbranch_vccz .LBB4_198
	s_and_b64 vcc, exec, s[26:27]
	s_cbranch_vccz .LBB4_199

.LBB4_154:
	s_barrier
	s_waitcnt lgkmcnt(0)
	ds_read_b128 v[82:85], v138 offset:20480
	ds_read_b128 v[86:89], v138 offset:22528
	ds_read_b128 v[90:93], v137
	s_and_b64 vcc, exec, s[24:25]
	s_waitcnt lgkmcnt(0)
	v_mfma_f32_16x16x32_f16 v[50:53], v[82:85], v[90:93], v[50:53]
	v_mfma_f32_16x16x32_f16 v[54:57], v[86:89], v[90:93], v[54:57]
	ds_read_b128 v[90:93], v137 offset:2048
	ds_read_b128 v[156:159], v137 offset:4096
	ds_read_b128 v[160:163], v137 offset:6144
	ds_read_b128 v[164:167], v137 offset:8192
	ds_read_b128 v[168:171], v137 offset:10240
	s_waitcnt lgkmcnt(4)
	v_mfma_f32_16x16x32_f16 v[18:21], v[82:85], v[90:93], v[18:21]
	v_mfma_f32_16x16x32_f16 v[22:25], v[86:89], v[90:93], v[22:25]
	s_waitcnt lgkmcnt(3)
	v_mfma_f32_16x16x32_f16 v[58:61], v[82:85], v[156:159], v[58:61]
	v_mfma_f32_16x16x32_f16 v[62:65], v[86:89], v[156:159], v[62:65]
	ds_read_b128 v[156:159], v137 offset:12288
	s_waitcnt lgkmcnt(3)
	v_mfma_f32_16x16x32_f16 v[26:29], v[82:85], v[160:163], v[26:29]
	v_mfma_f32_16x16x32_f16 v[30:33], v[86:89], v[160:163], v[30:33]
	ds_read_b128 v[160:163], v137 offset:14336
	s_waitcnt lgkmcnt(3)
	ds_read_b128 v[184:187], v137 offset:16384
	v_mfma_f32_16x16x32_f16 v[66:69], v[82:85], v[164:167], v[66:69]
	v_mfma_f32_16x16x32_f16 v[70:73], v[86:89], v[164:167], v[70:73]
	s_waitcnt lgkmcnt(3)
	v_mfma_f32_16x16x32_f16 v[34:37], v[82:85], v[168:171], v[34:37]
	v_mfma_f32_16x16x32_f16 v[38:41], v[86:89], v[168:171], v[38:41]
	s_waitcnt lgkmcnt(2)
	v_mfma_f32_16x16x32_f16 v[74:77], v[82:85], v[156:159], v[74:77]
	v_mfma_f32_16x16x32_f16 v[78:81], v[86:89], v[156:159], v[78:81]
	s_waitcnt lgkmcnt(1)
	v_mfma_f32_16x16x32_f16 v[42:45], v[82:85], v[160:163], v[42:45]
	v_mfma_f32_16x16x32_f16 v[46:49], v[86:89], v[160:163], v[46:49]
	s_cbranch_vccnz .LBB4_156
	s_waitcnt lgkmcnt(0)
	v_mfma_f32_16x16x32_f16 v[6:9], v[82:85], v[184:187], v[6:9]
	v_mfma_f32_16x16x32_f16 v[2:5], v[86:89], v[184:187], v[2:5]

.LBB4_158:
	s_waitcnt lgkmcnt(0)
	ds_read_b128 v[82:85], v139 offset:20480
	ds_read_b128 v[86:89], v139 offset:22528
	ds_read_b128 v[90:93], v0
	ds_read_b128 v[94:97], v0 offset:2048
	ds_read_b128 v[156:159], v0 offset:4096
	ds_read_b128 v[160:163], v0 offset:6144
	ds_read_b128 v[164:167], v0 offset:8192
	ds_read_b128 v[168:171], v0 offset:10240
	s_and_b64 vcc, exec, s[24:25]
	s_waitcnt lgkmcnt(5)
	v_mfma_f32_16x16x32_f16 v[50:53], v[82:85], v[90:93], v[50:53]
	v_mfma_f32_16x16x32_f16 v[54:57], v[86:89], v[90:93], v[54:57]
	s_waitcnt lgkmcnt(4)
	v_mfma_f32_16x16x32_f16 v[18:21], v[82:85], v[94:97], v[18:21]
	v_mfma_f32_16x16x32_f16 v[22:25], v[86:89], v[94:97], v[22:25]
	s_waitcnt lgkmcnt(3)
	v_mfma_f32_16x16x32_f16 v[58:61], v[82:85], v[156:159], v[58:61]
	v_mfma_f32_16x16x32_f16 v[62:65], v[86:89], v[156:159], v[62:65]
	ds_read_b128 v[156:159], v0 offset:12288
	s_waitcnt lgkmcnt(3)
	v_mfma_f32_16x16x32_f16 v[26:29], v[82:85], v[160:163], v[26:29]
	v_mfma_f32_16x16x32_f16 v[30:33], v[86:89], v[160:163], v[30:33]
	ds_read_b128 v[160:163], v0 offset:14336
	s_waitcnt lgkmcnt(3)
	ds_read_b128 v[184:187], v0 offset:16384
	v_mfma_f32_16x16x32_f16 v[66:69], v[82:85], v[164:167], v[66:69]
	v_mfma_f32_16x16x32_f16 v[70:73], v[86:89], v[164:167], v[70:73]
	s_waitcnt lgkmcnt(3)
	v_mfma_f32_16x16x32_f16 v[34:37], v[82:85], v[168:171], v[34:37]
	v_mfma_f32_16x16x32_f16 v[38:41], v[86:89], v[168:171], v[38:41]
	s_waitcnt lgkmcnt(2)
	v_mfma_f32_16x16x32_f16 v[74:77], v[82:85], v[156:159], v[74:77]
	v_mfma_f32_16x16x32_f16 v[78:81], v[86:89], v[156:159], v[78:81]
	s_waitcnt lgkmcnt(1)
	v_mfma_f32_16x16x32_f16 v[42:45], v[82:85], v[160:163], v[42:45]
	v_mfma_f32_16x16x32_f16 v[46:49], v[86:89], v[160:163], v[46:49]
	s_cbranch_vccnz .LBB4_160
	s_waitcnt lgkmcnt(0)
	v_mfma_f32_16x16x32_f16 v[6:9], v[82:85], v[184:187], v[6:9]
	v_mfma_f32_16x16x32_f16 v[2:5], v[86:89], v[184:187], v[2:5]

.LBB4_166:
	ds_read_b128 v[114:117], v143 offset:53248
	ds_read_b128 v[118:121], v143 offset:55296
	ds_read_b128 v[42:45], v0 offset:53248
	ds_read_b128 v[46:49], v0 offset:55296
	s_load_dwordx2 s[0:1], s[0:1], 0x10
	s_and_b64 vcc, exec, s[24:25]
	s_waitcnt lgkmcnt(0)
	v_mfma_f32_16x16x32_f16 v[74:77], v[114:117], v[42:45], v[50:53]
	v_mfma_f32_16x16x32_f16 v[78:81], v[118:121], v[42:45], v[54:57]
	v_mfma_f32_16x16x32_f16 v[66:69], v[114:117], v[46:49], v[94:97]
	v_mfma_f32_16x16x32_f16 v[70:73], v[118:121], v[46:49], v[98:101]
	ds_read_b128 v[42:45], v0 offset:57344
	ds_read_b128 v[46:49], v0 offset:59392
	s_waitcnt lgkmcnt(0)
	v_mfma_f32_16x16x32_f16 v[58:61], v[114:117], v[42:45], v[18:21]
	v_mfma_f32_16x16x32_f16 v[62:65], v[118:121], v[42:45], v[22:25]
	s_nop 1
	ds_read_b128 v[18:21], v0 offset:61440
	ds_read_b128 v[22:25], v0 offset:63488
	v_mfma_f32_16x16x32_f16 v[50:53], v[114:117], v[46:49], v[102:105]
	v_mfma_f32_16x16x32_f16 v[54:57], v[118:121], v[46:49], v[106:109]
	s_waitcnt lgkmcnt(0)
	ds_read_b128 v[184:187], v141 offset:16384
	v_mfma_f32_16x16x32_f16 v[42:45], v[114:117], v[18:21], v[26:29]
	v_mfma_f32_16x16x32_f16 v[46:49], v[118:121], v[18:21], v[30:33]
	v_mfma_f32_16x16x32_f16 v[34:37], v[114:117], v[22:25], v[34:37]
	v_mfma_f32_16x16x32_f16 v[38:41], v[118:121], v[22:25], v[38:41]
	ds_read_b128 v[18:21], v141 offset:12288
	ds_read_b128 v[22:25], v141 offset:14336
	s_waitcnt lgkmcnt(0)
	v_mfma_f32_16x16x32_f16 v[26:29], v[114:117], v[18:21], v[82:85]
	v_mfma_f32_16x16x32_f16 v[30:33], v[118:121], v[18:21], v[86:89]
	v_mfma_f32_16x16x32_f16 v[18:21], v[114:117], v[22:25], v[110:113]
	v_mfma_f32_16x16x32_f16 v[22:25], v[118:121], v[22:25], v[90:93]
	s_cbranch_vccnz .LBB4_168
	s_waitcnt lgkmcnt(0)
	v_mfma_f32_16x16x32_f16 v[6:9], v[114:117], v[184:187], v[6:9]
	v_mfma_f32_16x16x32_f16 v[2:5], v[118:121], v[184:187], v[2:5]

.LBB4_186:
	s_waitcnt lgkmcnt(0)
	v_mfma_f32_16x16x32_f16 v[6:9], v[102:105], v[184:187], v[6:9]
	v_mfma_f32_16x16x32_f16 v[2:5], v[106:109], v[184:187], v[2:5]
	v_cndmask_b32_e64 v82, 0, 1, s[28:29]
	v_cmp_ne_u32_e64 s[26:27], 1, v82
	s_andn2_b64 vcc, exec, s[28:29]
	s_cbranch_vccnz .LBB4_93

.LBB4_189:
	s_waitcnt lgkmcnt(0)
	v_mfma_f32_16x16x32_f16 v[6:9], v[98:101], v[184:187], v[6:9]
	v_mfma_f32_16x16x32_f16 v[2:5], v[102:105], v[184:187], v[2:5]
	s_and_b64 vcc, exec, s[26:27]
	s_cbranch_vccnz .LBB4_104

.LBB4_192:
	s_waitcnt lgkmcnt(0)
	v_mfma_f32_16x16x32_f16 v[6:9], v[82:85], v[184:187], v[6:9]
	v_mfma_f32_16x16x32_f16 v[2:5], v[86:89], v[184:187], v[2:5]
	s_and_b64 vcc, exec, s[26:27]
	s_cbranch_vccnz .LBB4_129

.LBB4_198:
	s_waitcnt lgkmcnt(0)
	v_mfma_f32_16x16x32_f16 v[6:9], v[114:117], v[184:187], v[6:9]
	v_mfma_f32_16x16x32_f16 v[2:5], v[118:121], v[184:187], v[2:5]
	s_and_b64 vcc, exec, s[26:27]
	s_cbranch_vccnz .LBB4_151

	.amdhsa_kernel _Z8moe_gemmILi2EEvPKDF16_S1_PvPKyPKiPKfS1_
		.amdhsa_group_segment_fixed_size 0
		.amdhsa_private_segment_fixed_size 0
		.amdhsa_kernarg_size 56
		.amdhsa_user_sgpr_count 2
		.amdhsa_user_sgpr_dispatch_ptr 0
		.amdhsa_user_sgpr_queue_ptr 0
		.amdhsa_user_sgpr_kernarg_segment_ptr 1
		.amdhsa_user_sgpr_dispatch_id 0
		.amdhsa_user_sgpr_kernarg_preload_length 0
		.amdhsa_user_sgpr_kernarg_preload_offset 0
		.amdhsa_user_sgpr_private_segment_size 0
		.amdhsa_uses_dynamic_stack 0
		.amdhsa_enable_private_segment 0
		.amdhsa_system_sgpr_workgroup_id_x 1
		.amdhsa_system_sgpr_workgroup_id_y 0
		.amdhsa_system_sgpr_workgroup_id_z 0
		.amdhsa_system_sgpr_workgroup_info 0
		.amdhsa_system_vgpr_workitem_id 0
		.amdhsa_next_free_vgpr 188
		.amdhsa_next_free_sgpr 94
		.amdhsa_accum_offset 188
		.amdhsa_reserve_vcc 1
		.amdhsa_float_round_mode_32 0
		.amdhsa_float_round_mode_16_64 0
		.amdhsa_float_denorm_mode_32 3
		.amdhsa_float_denorm_mode_16_64 3
		.amdhsa_dx10_clamp 1
		.amdhsa_ieee_mode 1
		.amdhsa_fp16_overflow 0
		.amdhsa_tg_split 0
		.amdhsa_exception_fp_ieee_invalid_op 0
		.amdhsa_exception_fp_denorm_src 0
		.amdhsa_exception_fp_ieee_div_zero 0
		.amdhsa_exception_fp_ieee_overflow 0
		.amdhsa_exception_fp_ieee_underflow 0
		.amdhsa_exception_fp_ieee_inexact 0
		.amdhsa_exception_int_div_zero 0
	.end_amdhsa_kernel

amdhsa.kernels:
  - .agpr_count:     0
    .args:
      - .actual_access:  write_only
        .address_space:  global
        .offset:         0
        .size:           8
        .value_kind:     global_buffer
    .group_segment_fixed_size: 0
    .kernarg_segment_align: 8
    .kernarg_segment_size: 8
    .language:       OpenCL C
    .language_version:
      - 2
      - 0
    .max_flat_workgroup_size: 1024
    .name:           _Z15zero_cnt_kernelPy
    .private_segment_fixed_size: 0
    .sgpr_count:     10
    .sgpr_spill_count: 0
    .symbol:         _Z15zero_cnt_kernelPy.kd
    .uniform_work_group_size: 1
    .uses_dynamic_stack: false
    .vgpr_count:     3
    .vgpr_spill_count: 0
    .wavefront_size: 64
  - .agpr_count:     0
    .args:
      - .actual_access:  read_only
        .address_space:  global
        .offset:         0
        .size:           8
        .value_kind:     global_buffer
      - .actual_access:  read_only
        .address_space:  global
        .offset:         8
        .size:           8
        .value_kind:     global_buffer
      - .actual_access:  read_only
        .address_space:  global
        .offset:         16
        .size:           8
        .value_kind:     global_buffer
      - .actual_access:  read_only
        .address_space:  global
        .offset:         24
        .size:           8
        .value_kind:     global_buffer
      - .actual_access:  write_only
        .address_space:  global
        .offset:         32
        .size:           8
        .value_kind:     global_buffer
      - .actual_access:  write_only
        .address_space:  global
        .offset:         40
        .size:           8
        .value_kind:     global_buffer
      - .actual_access:  write_only
        .address_space:  global
        .offset:         48
        .size:           8
        .value_kind:     global_buffer
      - .address_space:  global
        .offset:         56
        .size:           8
        .value_kind:     global_buffer
      - .actual_access:  write_only
        .address_space:  global
        .offset:         64
        .size:           8
        .value_kind:     global_buffer
      - .actual_access:  write_only
        .address_space:  global
        .offset:         72
        .size:           8
        .value_kind:     global_buffer
    .group_segment_fixed_size: 0
    .kernarg_segment_align: 8
    .kernarg_segment_size: 80
    .language:       OpenCL C
    .language_version:
      - 2
      - 0
    .max_flat_workgroup_size: 256
    .name:           _Z11prep_kernelPKfS0_S0_S0_PDF16_S1_S1_PyPiPf
    .private_segment_fixed_size: 0
    .sgpr_count:     55
    .sgpr_spill_count: 0
    .symbol:         _Z11prep_kernelPKfS0_S0_S0_PDF16_S1_S1_PyPiPf.kd
    .uniform_work_group_size: 1
    .uses_dynamic_stack: false
    .vgpr_count:     248
    .vgpr_spill_count: 0
    .wavefront_size: 64
  - .agpr_count:     0
    .args:
      - .address_space:  global
        .offset:         0
        .size:           8
        .value_kind:     global_buffer
      - .address_space:  global
        .offset:         8
        .size:           8
        .value_kind:     global_buffer
      - .actual_access:  write_only
        .address_space:  global
        .offset:         16
        .size:           8
        .value_kind:     global_buffer
      - .actual_access:  read_only
        .address_space:  global
        .offset:         24
        .size:           8
        .value_kind:     global_buffer
      - .actual_access:  read_only
        .address_space:  global
        .offset:         32
        .size:           8
        .value_kind:     global_buffer
      - .actual_access:  read_only
        .address_space:  global
        .offset:         40
        .size:           8
        .value_kind:     global_buffer
      - .actual_access:  read_only
        .address_space:  global
        .offset:         48
        .size:           8
        .value_kind:     global_buffer
    .group_segment_fixed_size: 0
    .kernarg_segment_align: 8
    .kernarg_segment_size: 56
    .language:       OpenCL C
    .language_version:
      - 2
      - 0
    .max_flat_workgroup_size: 512
    .name:           _Z8moe_gemmILi0EEvPKDF16_S1_PvPKyPKiPKfS1_
    .private_segment_fixed_size: 0
    .sgpr_count:     98
    .sgpr_spill_count: 0
    .symbol:         _Z8moe_gemmILi0EEvPKDF16_S1_PvPKyPKiPKfS1_.kd
    .uniform_work_group_size: 1
    .uses_dynamic_stack: false
    .vgpr_count:     256
    .vgpr_spill_count: 0
    .wavefront_size: 64
  - .agpr_count:     0
    .args:
      - .address_space:  global
        .offset:         0
        .size:           8
        .value_kind:     global_buffer
      - .address_space:  global
        .offset:         8
        .size:           8
        .value_kind:     global_buffer
      - .actual_access:  write_only
        .address_space:  global
        .offset:         16
        .size:           8
        .value_kind:     global_buffer
      - .actual_access:  read_only
        .address_space:  global
        .offset:         24
        .size:           8
        .value_kind:     global_buffer
      - .actual_access:  read_only
        .address_space:  global
        .offset:         32
        .size:           8
        .value_kind:     global_buffer
      - .actual_access:  read_only
        .address_space:  global
        .offset:         40
        .size:           8
        .value_kind:     global_buffer
      - .actual_access:  read_only
        .address_space:  global
        .offset:         48
        .size:           8
        .value_kind:     global_buffer
    .group_segment_fixed_size: 0
    .kernarg_segment_align: 8
    .kernarg_segment_size: 56
    .language:       OpenCL C
    .language_version:
      - 2
      - 0
    .max_flat_workgroup_size: 512
    .name:           _Z8moe_gemmILi1EEvPKDF16_S1_PvPKyPKiPKfS1_
    .private_segment_fixed_size: 0
    .sgpr_count:     100
    .sgpr_spill_count: 0
    .symbol:         _Z8moe_gemmILi1EEvPKDF16_S1_PvPKyPKiPKfS1_.kd
    .uniform_work_group_size: 1
    .uses_dynamic_stack: false
    .vgpr_count:     180
    .vgpr_spill_count: 0
    .wavefront_size: 64
  - .agpr_count:     0
    .args:
      - .address_space:  global
        .offset:         0
        .size:           8
        .value_kind:     global_buffer
      - .address_space:  global
        .offset:         8
        .size:           8
        .value_kind:     global_buffer
      - .actual_access:  write_only
        .address_space:  global
        .offset:         16
        .size:           8
        .value_kind:     global_buffer
      - .actual_access:  read_only
        .address_space:  global
        .offset:         24
        .size:           8
        .value_kind:     global_buffer
      - .actual_access:  read_only
        .address_space:  global
        .offset:         32
        .size:           8
        .value_kind:     global_buffer
      - .actual_access:  read_only
        .address_space:  global
        .offset:         40
        .size:           8
        .value_kind:     global_buffer
      - .actual_access:  read_only
        .address_space:  global
        .offset:         48
        .size:           8
        .value_kind:     global_buffer
    .group_segment_fixed_size: 0
    .kernarg_segment_align: 8
    .kernarg_segment_size: 56
    .language:       OpenCL C
    .language_version:
      - 2
      - 0
    .max_flat_workgroup_size: 512
    .name:           _Z8moe_gemmILi2EEvPKDF16_S1_PvPKyPKiPKfS1_
    .private_segment_fixed_size: 0
    .sgpr_count:     100
    .sgpr_spill_count: 0
    .symbol:         _Z8moe_gemmILi2EEvPKDF16_S1_PvPKyPKiPKfS1_.kd
    .uniform_work_group_size: 1
    .uses_dynamic_stack: false
    .vgpr_count:     188
    .vgpr_spill_count: 0
    .wavefront_size: 64
